# phase 8 software-pipelined: routing records of a wave's four tokens read once, next token's 24 row loads issued before the current token is combined
# baseline (speedup 1.0000x reference)
; __device__ __forceinline__ void phase12(const Args& a, unsigned char* lds_g, int lane, int wave) {
;     ...
; #pragma unroll 1
;       for (int t = t0; t < t0 + 4; ++t) {
;         const int4 q0 = ASG[2 * t], q1 = ASG[2 * t + 1];
;         const float w0 = __int_as_float(q0.z), w1 = __int_as_float(q1.z);
;         const unsigned long long* xr = (const unsigned long long*)(X1 + (size_t)t * D) + lane;
;         const unsigned* y0 = (const unsigned*)(Y2 + (size_t)(256 * cum[q0.x] + q0.y) * D) + lane; const unsigned* y1 = (const unsigned*)(Y2 + (size_t)(256 * cum[q1.x] + q1.y) * D) + lane;
;         f32x4 v[8]; float s = 0.f;
; #pragma unroll
;         for (int j = 0; j < 8; ++j) {
;             const int c = 4 * lane + 256 * j;
;             const f32x4 g2 = g2v[j]; (void)c;
;             const unsigned a0 = y0[64 * j], a1 = y1[64 * j];
;             const auto l0 = __builtin_amdgcn_cvt_pk_f32_fp8((int)a0, false), h0 = __builtin_amdgcn_cvt_pk_f32_fp8((int)a0, true), l1 = __builtin_amdgcn_cvt_pk_f32_fp8((int)a1, false), h1 = __builtin_amdgcn_cvt_pk_f32_fp8((int)a1, true);
;             f32x4 y; y.x = w0 * l0[0] + w1 * l1[0]; y.y = w0 * l0[1] + w1 * l1[1]; y.z = w0 * h0[0] + w1 * h1[0]; y.w = w0 * h0[1] + w1 * h1[1];
;             const unsigned long long xw = xr[64 * j];
.LBB0_1278:
	s_or_b32 s29, s8, 3
	v_mov_b64_e32 v[82:83], v[80:81]
	v_mov_b64_e32 v[84:85], v[78:79]
	s_mov_b32 s20, s27
	s_mov_b32 s30, s26
	s_ashr_i32 s21, s20, 31
	s_lshl_b64 s[0:1], s[20:21], 4
	s_add_u32 s0, s24, s0
	s_addc_u32 s1, s25, s1
	global_load_dwordx3 v[196:198], v65, s[0:1]
	global_load_dwordx3 v[200:202], v65, s[0:1] offset:16
	global_load_dwordx3 v[204:206], v65, s[0:1] offset:32
	global_load_dwordx3 v[208:210], v65, s[0:1] offset:48
	global_load_dwordx3 v[212:214], v65, s[0:1] offset:64
	global_load_dwordx3 v[216:218], v65, s[0:1] offset:80
	global_load_dwordx3 v[220:222], v65, s[0:1] offset:96
	global_load_dwordx3 v[224:226], v65, s[0:1] offset:112
	s_waitcnt vmcnt(0)
	v_lshl_add_u32 v199, v196, 2, s9
	v_lshl_add_u32 v203, v200, 2, s9
	v_lshl_add_u32 v207, v204, 2, s9
	v_lshl_add_u32 v211, v208, 2, s9
	v_lshl_add_u32 v215, v212, 2, s9
	v_lshl_add_u32 v219, v216, 2, s9
	v_lshl_add_u32 v223, v220, 2, s9
	v_lshl_add_u32 v227, v224, 2, s9
	ds_read_b32 v199, v199
	ds_read_b32 v203, v203
	ds_read_b32 v207, v207
	ds_read_b32 v211, v211
	ds_read_b32 v215, v215
	ds_read_b32 v219, v219
	ds_read_b32 v223, v223
	ds_read_b32 v227, v227
	s_waitcnt lgkmcnt(0)
	v_lshl_add_u32 v199, v199, 8, v197
	v_lshlrev_b32_e32 v228, 11, v199
	v_mov_b32_e32 v230, v198
	v_lshl_add_u32 v203, v203, 8, v201
	v_lshlrev_b32_e32 v229, 11, v203
	v_mov_b32_e32 v231, v202
	v_lshl_add_u32 v207, v207, 8, v205
	v_lshlrev_b32_e32 v232, 11, v207
	v_mov_b32_e32 v234, v206
	v_lshl_add_u32 v211, v211, 8, v209
	v_lshlrev_b32_e32 v233, 11, v211
	v_mov_b32_e32 v235, v210
	v_lshl_add_u32 v215, v215, 8, v213
	v_lshlrev_b32_e32 v236, 11, v215
	v_mov_b32_e32 v238, v214
	v_lshl_add_u32 v219, v219, 8, v217
	v_lshlrev_b32_e32 v237, 11, v219
	v_mov_b32_e32 v239, v218
	v_lshl_add_u32 v223, v223, 8, v221
	v_lshlrev_b32_e32 v240, 11, v223
	v_mov_b32_e32 v242, v222
	v_lshl_add_u32 v227, v227, 8, v225
	v_lshlrev_b32_e32 v241, 11, v227
	v_mov_b32_e32 v243, v226
	global_load_dwordx2 v[86:87], v[82:83], off offset:-2048
	global_load_dwordx2 v[88:89], v[82:83], off offset:-1536
	global_load_dwordx2 v[90:91], v[82:83], off offset:-1024
	global_load_dwordx2 v[92:93], v[82:83], off offset:-512
	global_load_dwordx2 v[94:95], v[82:83], off
	global_load_dwordx2 v[96:97], v[82:83], off offset:512
	global_load_dwordx2 v[116:117], v[82:83], off offset:1024
	global_load_dwordx2 v[118:119], v[82:83], off offset:1536
	v_lshl_add_u64 v[82:83], v[82:83], 0, s[12:13]
	v_add_co_u32_e32 v244, vcc, v68, v228
	s_nop 1
	v_addc_co_u32_e32 v245, vcc, 0, v69, vcc
	v_add_co_u32_e32 v246, vcc, v68, v229
	s_nop 1
	v_addc_co_u32_e32 v247, vcc, 0, v69, vcc
	global_load_dword v107, v[244:245], off
	global_load_dword v109, v[246:247], off
	global_load_dword v111, v[244:245], off offset:256
	global_load_dword v146, v[246:247], off offset:256
	global_load_dword v150, v[244:245], off offset:512
	global_load_dword v154, v[246:247], off offset:512
	global_load_dword v158, v[244:245], off offset:768
	global_load_dword v162, v[246:247], off offset:768
	global_load_dword v166, v[244:245], off offset:1024
	global_load_dword v170, v[246:247], off offset:1024
	global_load_dword v174, v[244:245], off offset:1280
	global_load_dword v178, v[246:247], off offset:1280
	global_load_dword v182, v[244:245], off offset:1536
	global_load_dword v186, v[246:247], off offset:1536
	global_load_dword v190, v[244:245], off offset:1792
	global_load_dword v194, v[246:247], off offset:1792
	global_load_dwordx2 v[196:197], v[82:83], off offset:-2048
	global_load_dwordx2 v[198:199], v[82:83], off offset:-1536
	global_load_dwordx2 v[200:201], v[82:83], off offset:-1024
	global_load_dwordx2 v[202:203], v[82:83], off offset:-512
	global_load_dwordx2 v[204:205], v[82:83], off
	global_load_dwordx2 v[206:207], v[82:83], off offset:512
	global_load_dwordx2 v[208:209], v[82:83], off offset:1024
	global_load_dwordx2 v[210:211], v[82:83], off offset:1536
	v_lshl_add_u64 v[82:83], v[82:83], 0, s[12:13]
	v_add_co_u32_e32 v244, vcc, v68, v232
	s_nop 1
	v_addc_co_u32_e32 v245, vcc, 0, v69, vcc
	v_add_co_u32_e32 v246, vcc, v68, v233
	s_nop 1
	v_addc_co_u32_e32 v247, vcc, 0, v69, vcc
	global_load_dword v212, v[244:245], off
	global_load_dword v213, v[246:247], off
	global_load_dword v214, v[244:245], off offset:256
	global_load_dword v215, v[246:247], off offset:256
	global_load_dword v216, v[244:245], off offset:512
	global_load_dword v217, v[246:247], off offset:512
	global_load_dword v218, v[244:245], off offset:768
	global_load_dword v219, v[246:247], off offset:768
	global_load_dword v220, v[244:245], off offset:1024
	global_load_dword v221, v[246:247], off offset:1024
	global_load_dword v222, v[244:245], off offset:1280
	global_load_dword v223, v[246:247], off offset:1280
	global_load_dword v224, v[244:245], off offset:1536
	global_load_dword v225, v[246:247], off offset:1536
	global_load_dword v226, v[244:245], off offset:1792
	global_load_dword v227, v[246:247], off offset:1792
	s_waitcnt vmcnt(24)
; __device__ __forceinline__ void phase12(const Args& a, unsigned char* lds_g, int lane, int wave) {
;     ...
;         for (int j = 0; j < 8; ++j) {
;             const int c = 4 * lane + 256 * j;
;             const f32x4 g2 = g2v[j]; (void)c;
;             const unsigned a0 = y0[64 * j], a1 = y1[64 * j];
;             const auto l0 = __builtin_amdgcn_cvt_pk_f32_fp8((int)a0, false), h0 = __builtin_amdgcn_cvt_pk_f32_fp8((int)a0, true), l1 = __builtin_amdgcn_cvt_pk_f32_fp8((int)a1, false), h1 = __builtin_amdgcn_cvt_pk_f32_fp8((int)a1, true);
;             f32x4 y; y.x = w0 * l0[0] + w1 * l1[0]; y.y = w0 * l0[1] + w1 * l1[1]; y.z = w0 * h0[0] + w1 * h1[0]; y.w = w0 * h0[1] + w1 * h1[1];
;             const unsigned long long xw = xr[64 * j];
;             v[j] = (f32x4){bflo((unsigned)xw), bfhi((unsigned)xw), bflo((unsigned)(xw >> 32)), bfhi((unsigned)(xw >> 32))} + g2 * y;
	v_mov_b32_e32 v110, v230
	v_mov_b32_e32 v108, v231
	v_lshlrev_b32_e32 v120, 16, v86
	v_and_b32_e32 v121, 0xffff0000, v86
	v_lshlrev_b32_e32 v86, 16, v87
	v_and_b32_e32 v87, 0xffff0000, v87
	v_lshlrev_b32_e32 v122, 16, v88
	v_and_b32_e32 v123, 0xffff0000, v88
	v_lshlrev_b32_e32 v88, 16, v89
	v_and_b32_e32 v89, 0xffff0000, v89
	v_lshlrev_b32_e32 v124, 16, v90
	v_and_b32_e32 v125, 0xffff0000, v90
	v_lshlrev_b32_e32 v90, 16, v91
	v_and_b32_e32 v91, 0xffff0000, v91
	v_lshlrev_b32_e32 v126, 16, v92
	v_and_b32_e32 v127, 0xffff0000, v92
	v_lshlrev_b32_e32 v130, 16, v96
	v_and_b32_e32 v131, 0xffff0000, v96
	v_lshlrev_b32_e32 v134, 16, v118
	v_and_b32_e32 v135, 0xffff0000, v118
	v_lshlrev_b32_e32 v128, 16, v94
	v_and_b32_e32 v129, 0xffff0000, v94
	v_lshlrev_b32_e32 v132, 16, v116
	v_and_b32_e32 v133, 0xffff0000, v116
	v_lshlrev_b32_e32 v118, 16, v119
	v_and_b32_e32 v119, 0xffff0000, v119
	v_lshlrev_b32_e32 v92, 16, v93
	v_and_b32_e32 v93, 0xffff0000, v93
	v_lshlrev_b32_e32 v96, 16, v97
	v_and_b32_e32 v97, 0xffff0000, v97
	v_lshlrev_b32_e32 v94, 16, v95
	v_and_b32_e32 v95, 0xffff0000, v95
	v_lshlrev_b32_e32 v116, 16, v117
	v_and_b32_e32 v117, 0xffff0000, v117
	v_cvt_pk_f32_fp8_e32 v[112:113], v107
	v_cvt_pk_f32_fp8_e32 v[136:137], v109
	v_cvt_pk_f32_fp8_sdwa v[138:139], v109 src0_sel:WORD_1
	v_cvt_pk_f32_fp8_e32 v[144:145], v146
	v_cvt_pk_f32_fp8_sdwa v[146:147], v146 src0_sel:WORD_1
	v_cvt_pk_f32_fp8_sdwa v[114:115], v107 src0_sel:WORD_1
	v_cvt_pk_f32_fp8_e32 v[140:141], v111
	v_cvt_pk_f32_fp8_sdwa v[142:143], v111 src0_sel:WORD_1
	v_cvt_pk_f32_fp8_e32 v[152:153], v154
	v_cvt_pk_f32_fp8_sdwa v[154:155], v154 src0_sel:WORD_1
	v_cvt_pk_f32_fp8_e32 v[160:161], v162
	v_cvt_pk_f32_fp8_sdwa v[162:163], v162 src0_sel:WORD_1
	v_cvt_pk_f32_fp8_e32 v[168:169], v170
	v_cvt_pk_f32_fp8_sdwa v[170:171], v170 src0_sel:WORD_1
	v_cvt_pk_f32_fp8_e32 v[176:177], v178
	v_cvt_pk_f32_fp8_sdwa v[178:179], v178 src0_sel:WORD_1
	v_cvt_pk_f32_fp8_e32 v[184:185], v186
	v_cvt_pk_f32_fp8_sdwa v[186:187], v186 src0_sel:WORD_1
	v_cvt_pk_f32_fp8_e32 v[192:193], v194
	v_cvt_pk_f32_fp8_sdwa v[194:195], v194 src0_sel:WORD_1
	v_cvt_pk_f32_fp8_e32 v[148:149], v150
	v_cvt_pk_f32_fp8_sdwa v[150:151], v150 src0_sel:WORD_1
	v_cvt_pk_f32_fp8_e32 v[156:157], v158
	v_cvt_pk_f32_fp8_e32 v[172:173], v174
	v_cvt_pk_f32_fp8_e32 v[188:189], v190
	v_cvt_pk_f32_fp8_sdwa v[158:159], v158 src0_sel:WORD_1
	v_cvt_pk_f32_fp8_e32 v[164:165], v166
	v_cvt_pk_f32_fp8_sdwa v[166:167], v166 src0_sel:WORD_1
	v_cvt_pk_f32_fp8_sdwa v[174:175], v174 src0_sel:WORD_1
	v_cvt_pk_f32_fp8_e32 v[180:181], v182
	v_cvt_pk_f32_fp8_sdwa v[182:183], v182 src0_sel:WORD_1
	v_cvt_pk_f32_fp8_sdwa v[190:191], v190 src0_sel:WORD_1
	v_pk_mul_f32 v[138:139], v[108:109], v[138:139] op_sel_hi:[0,1]
	v_pk_mul_f32 v[136:137], v[108:109], v[136:137] op_sel_hi:[0,1]
	v_pk_mul_f32 v[146:147], v[108:109], v[146:147] op_sel_hi:[0,1]
	v_pk_mul_f32 v[144:145], v[108:109], v[144:145] op_sel_hi:[0,1]
	v_pk_mul_f32 v[152:153], v[108:109], v[152:153] op_sel_hi:[0,1]
	v_pk_mul_f32 v[154:155], v[108:109], v[154:155] op_sel_hi:[0,1]
	v_pk_mul_f32 v[162:163], v[108:109], v[162:163] op_sel_hi:[0,1]
	v_pk_mul_f32 v[160:161], v[108:109], v[160:161] op_sel_hi:[0,1]
	v_pk_mul_f32 v[170:171], v[108:109], v[170:171] op_sel_hi:[0,1]
	v_pk_mul_f32 v[168:169], v[108:109], v[168:169] op_sel_hi:[0,1]
	v_pk_mul_f32 v[176:177], v[108:109], v[176:177] op_sel_hi:[0,1]
	v_pk_mul_f32 v[178:179], v[108:109], v[178:179] op_sel_hi:[0,1]
	v_pk_mul_f32 v[186:187], v[108:109], v[186:187] op_sel_hi:[0,1]
	v_pk_mul_f32 v[184:185], v[108:109], v[184:185] op_sel_hi:[0,1]
	v_pk_mul_f32 v[194:195], v[108:109], v[194:195] op_sel_hi:[0,1]
	v_pk_mul_f32 v[108:109], v[108:109], v[192:193] op_sel_hi:[0,1]
	v_pk_fma_f32 v[112:113], v[110:111], v[112:113], v[136:137] op_sel_hi:[0,1,1]
	v_pk_fma_f32 v[114:115], v[110:111], v[114:115], v[138:139] op_sel_hi:[0,1,1]
	v_pk_fma_f32 v[136:137], v[110:111], v[140:141], v[144:145] op_sel_hi:[0,1,1]
	v_pk_fma_f32 v[138:139], v[110:111], v[142:143], v[146:147] op_sel_hi:[0,1,1]
	v_pk_fma_f32 v[140:141], v[110:111], v[150:151], v[154:155] op_sel_hi:[0,1,1]
	v_pk_fma_f32 v[142:143], v[110:111], v[148:149], v[152:153] op_sel_hi:[0,1,1]
	v_pk_fma_f32 v[144:145], v[110:111], v[156:157], v[160:161] op_sel_hi:[0,1,1]
	v_pk_fma_f32 v[154:155], v[110:111], v[172:173], v[176:177] op_sel_hi:[0,1,1]
	v_pk_fma_f32 v[108:109], v[110:111], v[188:189], v[108:109] op_sel_hi:[0,1,1]
	v_pk_fma_f32 v[86:87], v[10:11], v[114:115], v[86:87]
	v_pk_fma_f32 v[112:113], v[8:9], v[112:113], v[120:121]
	v_pk_fma_f32 v[88:89], v[14:15], v[138:139], v[88:89]
	v_pk_fma_f32 v[114:115], v[12:13], v[136:137], v[122:123]
	v_pk_fma_f32 v[146:147], v[110:111], v[158:159], v[162:163] op_sel_hi:[0,1,1]
	v_pk_fma_f32 v[148:149], v[110:111], v[164:165], v[168:169] op_sel_hi:[0,1,1]
	v_pk_fma_f32 v[150:151], v[110:111], v[166:167], v[170:171] op_sel_hi:[0,1,1]
	v_pk_fma_f32 v[152:153], v[110:111], v[174:175], v[178:179] op_sel_hi:[0,1,1]
	v_pk_fma_f32 v[156:157], v[110:111], v[180:181], v[184:185] op_sel_hi:[0,1,1]
	v_pk_fma_f32 v[158:159], v[110:111], v[182:183], v[186:187] op_sel_hi:[0,1,1]
	v_pk_fma_f32 v[110:111], v[110:111], v[190:191], v[194:195] op_sel_hi:[0,1,1]
	v_pk_fma_f32 v[120:121], v[20:21], v[142:143], v[124:125]
	v_pk_fma_f32 v[90:91], v[22:23], v[140:141], v[90:91]
	v_pk_fma_f32 v[122:123], v[28:29], v[144:145], v[126:127]
	v_pk_fma_f32 v[126:127], v[44:45], v[154:155], v[130:131]
	v_pk_fma_f32 v[108:109], v[60:61], v[108:109], v[134:135]
	v_mov_b32_e32 v130, v113
	v_mov_b32_e32 v131, v115
	v_mov_b32_e32 v134, v87
	v_mov_b32_e32 v135, v89
; __device__ __forceinline__ void phase12(const Args& a, unsigned char* lds_g, int lane, int wave) {
;     ...
;             s += (v[j].x * v[j].x + v[j].y * v[j].y) + (v[j].z * v[j].z + v[j].w * v[j].w);
;         }
;         const float rstd = 1.f / sqrtf(wave_sum(s) * (1.f / D) + EPS);
;         f32x4* o = (f32x4*)(a.out + (size_t)t * D) + lane;
; #pragma unroll
;         for (int j = 0; j < 8; ++j) o[64 * j] = v[j] * rstd * fgv[j];
	v_pk_fma_f32 v[124:125], v[36:37], v[148:149], v[128:129]
	v_pk_fma_f32 v[128:129], v[52:53], v[156:157], v[132:133]
	v_pk_fma_f32 v[110:111], v[62:63], v[110:111], v[118:119]
	v_mov_b32_e32 v118, v112
	v_mov_b32_e32 v119, v114
	v_mov_b32_e32 v132, v86
	v_mov_b32_e32 v133, v88
	v_pk_mul_f32 v[136:137], v[90:91], v[90:91]
	v_pk_mul_f32 v[138:139], v[120:121], v[120:121]
	v_pk_mul_f32 v[130:131], v[130:131], v[130:131]
	v_pk_mul_f32 v[134:135], v[134:135], v[134:135]
	v_pk_fma_f32 v[92:93], v[30:31], v[146:147], v[92:93]
	v_pk_fma_f32 v[96:97], v[46:47], v[152:153], v[96:97]
	v_pk_mov_b32 v[152:153], v[138:139], v[136:137] op_sel:[1,0]
	v_mov_b32_e32 v139, v137
	v_pk_fma_f32 v[118:119], v[118:119], v[118:119], v[130:131]
	v_pk_fma_f32 v[130:131], v[132:133], v[132:133], v[134:135]
	v_pk_fma_f32 v[94:95], v[38:39], v[150:151], v[94:95]
	v_mul_f32_e32 v140, v123, v123
	v_mul_f32_e32 v142, v93, v93
	v_pk_add_f32 v[132:133], v[152:153], v[138:139]
	v_pk_add_f32 v[118:119], v[118:119], v[130:131]
	v_mul_f32_e32 v107, v124, v124
	v_mul_f32_e32 v151, v125, v125
	v_mul_f32_e32 v154, v94, v94
	v_mul_f32_e32 v155, v95, v95
	v_pk_fma_f32 v[136:137], v[122:123], v[122:123], v[140:141] op_sel_hi:[1,1,0]
	v_pk_fma_f32 v[140:141], v[92:93], v[92:93], v[142:143] op_sel_hi:[1,1,0]
	v_pk_add_f32 v[130:131], v[132:133], v[132:133] op_sel:[0,1] op_sel_hi:[1,0]
	v_pk_add_f32 v[118:119], v[118:119], v[118:119] op_sel:[0,1] op_sel_hi:[1,0]
	v_pk_mul_f32 v[144:145], v[96:97], v[96:97]
	v_pk_mul_f32 v[146:147], v[126:127], v[126:127]
	v_mov_b32_e32 v137, v154
	v_mov_b32_e32 v141, v155
	v_mov_b32_e32 v131, v151
	v_mov_b32_e32 v119, v107
	v_pk_fma_f32 v[116:117], v[54:55], v[158:159], v[116:117]
	v_pk_mov_b32 v[142:143], v[146:147], v[144:145] op_sel:[1,0]
	v_mov_b32_e32 v147, v145
	v_pk_add_f32 v[132:133], v[136:137], v[140:141]
	v_pk_add_f32 v[118:119], v[118:119], v[130:131]
	v_mul_f32_e32 v148, v129, v129
	v_mul_f32_e32 v150, v117, v117
	v_pk_add_f32 v[134:135], v[142:143], v[146:147]
	v_pk_add_f32 v[118:119], v[118:119], v[132:133]
	v_mul_f32_e32 v156, v108, v108
	v_mul_f32_e32 v157, v109, v109
	v_mul_f32_e32 v158, v110, v110
	v_mul_f32_e32 v159, v111, v111
	v_pk_fma_f32 v[144:145], v[128:129], v[128:129], v[148:149] op_sel_hi:[1,1,0]
	v_pk_fma_f32 v[148:149], v[116:117], v[116:117], v[150:151] op_sel_hi:[1,1,0]
	v_pk_add_f32 v[134:135], v[134:135], v[134:135] op_sel:[0,1] op_sel_hi:[1,0]
	v_pk_add_f32 v[118:119], v[118:119], v[118:119] op_sel:[0,1] op_sel_hi:[1,0]
	v_mov_b32_e32 v145, v158
	v_mov_b32_e32 v149, v159
	v_mov_b32_e32 v135, v157
	v_mov_b32_e32 v119, v156
	v_pk_add_f32 v[136:137], v[144:145], v[148:149]
	v_pk_add_f32 v[118:119], v[118:119], v[134:135]
	s_nop 0
	v_pk_add_f32 v[118:119], v[118:119], v[136:137]
	s_nop 0
	v_add_f32_e32 v107, v118, v119
	ds_bpermute_b32 v118, v99, v107
	s_waitcnt lgkmcnt(0)
	v_add_f32_e32 v107, v107, v118
	ds_bpermute_b32 v118, v100, v107
	s_waitcnt lgkmcnt(0)
	v_add_f32_e32 v107, v107, v118
	ds_bpermute_b32 v118, v101, v107
	s_waitcnt lgkmcnt(0)
	v_add_f32_e32 v107, v107, v118
	ds_bpermute_b32 v118, v102, v107
	s_waitcnt lgkmcnt(0)
	v_add_f32_e32 v107, v107, v118
	ds_bpermute_b32 v118, v103, v107
	s_waitcnt lgkmcnt(0)
	v_add_f32_e32 v107, v107, v118
	ds_bpermute_b32 v118, v104, v107
	s_waitcnt lgkmcnt(0)
	v_add_f32_e32 v107, v107, v118
	v_fmamk_f32 v107, v107, 0x3a000000, v105
	v_mul_f32_e32 v118, 0x4f800000, v107
	v_cmp_gt_f32_e32 vcc, s11, v107
	s_nop 1
	v_cndmask_b32_e32 v107, v107, v118, vcc
	v_sqrt_f32_e32 v118, v107
	s_nop 0
	v_add_u32_e32 v119, -1, v118
	v_add_u32_e32 v130, 1, v118
	v_fma_f32 v131, -v119, v118, v107
	v_fma_f32 v132, -v130, v118, v107
	v_cmp_ge_f32_e64 s[0:1], 0, v131
	s_nop 1
	v_cndmask_b32_e64 v118, v118, v119, s[0:1]
	v_cmp_lt_f32_e64 s[0:1], 0, v132
	s_nop 1
	v_cndmask_b32_e64 v118, v118, v130, s[0:1]
	v_mul_f32_e32 v119, 0x37800000, v118
	v_cndmask_b32_e32 v118, v118, v119, vcc
	v_cmp_class_f32_e32 vcc, v107, v106
	s_nop 1
	v_cndmask_b32_e32 v107, v118, v107, vcc
	v_div_scale_f32 v118, s[0:1], v107, v107, 1.0
	v_rcp_f32_e32 v130, v118
	v_div_scale_f32 v119, vcc, 1.0, v107, 1.0
	v_fma_f32 v131, -v118, v130, 1.0
	v_fmac_f32_e32 v130, v131, v130
	v_mul_f32_e32 v131, v119, v130
	v_fma_f32 v132, -v118, v131, v119
	v_fmac_f32_e32 v131, v132, v130
	v_fma_f32 v118, -v118, v131, v119
	v_div_fmas_f32 v118, v118, v130, v131
	v_div_fixup_f32 v118, v118, v107, 1.0
	v_pk_mul_f32 v[112:113], v[112:113], v[118:119] op_sel_hi:[1,0]
	v_pk_mul_f32 v[86:87], v[86:87], v[118:119] op_sel_hi:[1,0]
	v_pk_mul_f32 v[114:115], v[114:115], v[118:119] op_sel_hi:[1,0]
	v_pk_mul_f32 v[130:131], v[88:89], v[118:119] op_sel_hi:[1,0]
	v_pk_mul_f32 v[120:121], v[120:121], v[118:119] op_sel_hi:[1,0]
	v_pk_mul_f32 v[132:133], v[90:91], v[118:119] op_sel_hi:[1,0]
	v_pk_mul_f32 v[122:123], v[122:123], v[118:119] op_sel_hi:[1,0]
	v_pk_mul_f32 v[134:135], v[92:93], v[118:119] op_sel_hi:[1,0]
	v_pk_mul_f32 v[124:125], v[124:125], v[118:119] op_sel_hi:[1,0]
	v_pk_mul_f32 v[136:137], v[94:95], v[118:119] op_sel_hi:[1,0]
	v_pk_mul_f32 v[126:127], v[126:127], v[118:119] op_sel_hi:[1,0]
	v_pk_mul_f32 v[138:139], v[96:97], v[118:119] op_sel_hi:[1,0]
	v_pk_mul_f32 v[128:129], v[128:129], v[118:119] op_sel_hi:[1,0]
	v_pk_mul_f32 v[140:141], v[116:117], v[118:119] op_sel_hi:[1,0]
	v_pk_mul_f32 v[142:143], v[108:109], v[118:119] op_sel_hi:[1,0]
	v_pk_mul_f32 v[144:145], v[110:111], v[118:119] op_sel_hi:[1,0]
	v_pk_mul_f32 v[88:89], v[2:3], v[86:87]
	v_pk_mul_f32 v[86:87], v[0:1], v[112:113]
	v_pk_mul_f32 v[92:93], v[6:7], v[130:131]
	v_pk_mul_f32 v[90:91], v[4:5], v[114:115]
	v_pk_mul_f32 v[96:97], v[18:19], v[132:133]
	v_pk_mul_f32 v[94:95], v[16:17], v[120:121]
	v_pk_mul_f32 v[110:111], v[26:27], v[134:135]
	v_pk_mul_f32 v[108:109], v[24:25], v[122:123]
	v_pk_mul_f32 v[114:115], v[34:35], v[136:137]
	v_pk_mul_f32 v[112:113], v[32:33], v[124:125]
	v_pk_mul_f32 v[118:119], v[42:43], v[138:139]
	v_pk_mul_f32 v[116:117], v[40:41], v[126:127]
	v_pk_mul_f32 v[122:123], v[50:51], v[140:141]
	v_pk_mul_f32 v[120:121], v[48:49], v[128:129]
	v_pk_mul_f32 v[126:127], v[58:59], v[144:145]
	v_pk_mul_f32 v[124:125], v[56:57], v[142:143]
	global_store_dwordx4 v[84:85], v[86:89], off offset:-4096 sc0 sc1
	global_store_dwordx4 v[84:85], v[90:93], off offset:-3072 sc0 sc1
	global_store_dwordx4 v[84:85], v[94:97], off offset:-2048 sc0 sc1
	global_store_dwordx4 v[84:85], v[108:111], off offset:-1024 sc0 sc1
	global_store_dwordx4 v[84:85], v[112:115], off sc0 sc1
	global_store_dwordx4 v[84:85], v[116:119], off offset:1024 sc0 sc1
	global_store_dwordx4 v[84:85], v[120:123], off offset:2048 sc0 sc1
	global_store_dwordx4 v[84:85], v[124:127], off offset:3072 sc0 sc1
	v_lshl_add_u64 v[84:85], v[84:85], 0, s[18:19]
	s_waitcnt vmcnt(8)
; __device__ __forceinline__ void phase12(const Args& a, unsigned char* lds_g, int lane, int wave) {
;     ...
;         const int4 q0 = ASG[2 * t], q1 = ASG[2 * t + 1];
;         const float w0 = __int_as_float(q0.z), w1 = __int_as_float(q1.z);
;         const unsigned long long* xr = (const unsigned long long*)(X1 + (size_t)t * D) + lane;
;         const unsigned* y0 = (const unsigned*)(Y2 + (size_t)(256 * cum[q0.x] + q0.y) * D) + lane; const unsigned* y1 = (const unsigned*)(Y2 + (size_t)(256 * cum[q1.x] + q1.y) * D) + lane;
;         f32x4 v[8]; float s = 0.f;
; #pragma unroll
;         for (int j = 0; j < 8; ++j) {
;             const int c = 4 * lane + 256 * j;
;             const f32x4 g2 = g2v[j]; (void)c;
;             const unsigned a0 = y0[64 * j], a1 = y1[64 * j];
;             const auto l0 = __builtin_amdgcn_cvt_pk_f32_fp8((int)a0, false), h0 = __builtin_amdgcn_cvt_pk_f32_fp8((int)a0, true), l1 = __builtin_amdgcn_cvt_pk_f32_fp8((int)a1, false), h1 = __builtin_amdgcn_cvt_pk_f32_fp8((int)a1, true);
;             f32x4 y; y.x = w0 * l0[0] + w1 * l1[0]; y.y = w0 * l0[1] + w1 * l1[1]; y.z = w0 * h0[0] + w1 * h1[0]; y.w = w0 * h0[1] + w1 * h1[1];
;             const unsigned long long xw = xr[64 * j];
;             v[j] = (f32x4){bflo((unsigned)xw), bfhi((unsigned)xw), bflo((unsigned)(xw >> 32)), bfhi((unsigned)(xw >> 32))} + g2 * y;
	v_mov_b64_e32 v[86:87], v[196:197]
	v_mov_b64_e32 v[88:89], v[198:199]
	v_mov_b64_e32 v[90:91], v[200:201]
	v_mov_b64_e32 v[92:93], v[202:203]
	v_mov_b64_e32 v[94:95], v[204:205]
	v_mov_b64_e32 v[96:97], v[206:207]
	v_mov_b64_e32 v[116:117], v[208:209]
	v_mov_b64_e32 v[118:119], v[210:211]
	v_mov_b32_e32 v107, v212
	v_mov_b32_e32 v109, v213
	v_mov_b32_e32 v111, v214
	v_mov_b32_e32 v146, v215
	v_mov_b32_e32 v150, v216
	v_mov_b32_e32 v154, v217
	v_mov_b32_e32 v158, v218
	v_mov_b32_e32 v162, v219
	v_mov_b32_e32 v166, v220
	v_mov_b32_e32 v170, v221
	v_mov_b32_e32 v174, v222
	v_mov_b32_e32 v178, v223
	v_mov_b32_e32 v182, v224
	v_mov_b32_e32 v186, v225
	v_mov_b32_e32 v190, v226
	v_mov_b32_e32 v194, v227
	global_load_dwordx2 v[196:197], v[82:83], off offset:-2048
	global_load_dwordx2 v[198:199], v[82:83], off offset:-1536
	global_load_dwordx2 v[200:201], v[82:83], off offset:-1024
	global_load_dwordx2 v[202:203], v[82:83], off offset:-512
	global_load_dwordx2 v[204:205], v[82:83], off
	global_load_dwordx2 v[206:207], v[82:83], off offset:512
	global_load_dwordx2 v[208:209], v[82:83], off offset:1024
	global_load_dwordx2 v[210:211], v[82:83], off offset:1536
	v_lshl_add_u64 v[82:83], v[82:83], 0, s[12:13]
	v_add_co_u32_e32 v244, vcc, v68, v236
	s_nop 1
	v_addc_co_u32_e32 v245, vcc, 0, v69, vcc
	v_add_co_u32_e32 v246, vcc, v68, v237
	s_nop 1
	v_addc_co_u32_e32 v247, vcc, 0, v69, vcc
	global_load_dword v212, v[244:245], off
	global_load_dword v213, v[246:247], off
	global_load_dword v214, v[244:245], off offset:256
	global_load_dword v215, v[246:247], off offset:256
	global_load_dword v216, v[244:245], off offset:512
	global_load_dword v217, v[246:247], off offset:512
	global_load_dword v218, v[244:245], off offset:768
	global_load_dword v219, v[246:247], off offset:768
	global_load_dword v220, v[244:245], off offset:1024
	global_load_dword v221, v[246:247], off offset:1024
	global_load_dword v222, v[244:245], off offset:1280
	global_load_dword v223, v[246:247], off offset:1280
	global_load_dword v224, v[244:245], off offset:1536
	global_load_dword v225, v[246:247], off offset:1536
	global_load_dword v226, v[244:245], off offset:1792
	global_load_dword v227, v[246:247], off offset:1792
	v_mov_b32_e32 v110, v234
	v_mov_b32_e32 v108, v235
	v_lshlrev_b32_e32 v120, 16, v86
	v_and_b32_e32 v121, 0xffff0000, v86
	v_lshlrev_b32_e32 v86, 16, v87
	v_and_b32_e32 v87, 0xffff0000, v87
	v_lshlrev_b32_e32 v122, 16, v88
	v_and_b32_e32 v123, 0xffff0000, v88
	v_lshlrev_b32_e32 v88, 16, v89
	v_and_b32_e32 v89, 0xffff0000, v89
	v_lshlrev_b32_e32 v124, 16, v90
	v_and_b32_e32 v125, 0xffff0000, v90
	v_lshlrev_b32_e32 v90, 16, v91
	v_and_b32_e32 v91, 0xffff0000, v91
	v_lshlrev_b32_e32 v126, 16, v92
	v_and_b32_e32 v127, 0xffff0000, v92
	v_lshlrev_b32_e32 v130, 16, v96
	v_and_b32_e32 v131, 0xffff0000, v96
	v_lshlrev_b32_e32 v134, 16, v118
	v_and_b32_e32 v135, 0xffff0000, v118
	v_lshlrev_b32_e32 v128, 16, v94
	v_and_b32_e32 v129, 0xffff0000, v94
	v_lshlrev_b32_e32 v132, 16, v116
	v_and_b32_e32 v133, 0xffff0000, v116
	v_lshlrev_b32_e32 v118, 16, v119
	v_and_b32_e32 v119, 0xffff0000, v119
	v_lshlrev_b32_e32 v92, 16, v93
	v_and_b32_e32 v93, 0xffff0000, v93
	v_lshlrev_b32_e32 v96, 16, v97
	v_and_b32_e32 v97, 0xffff0000, v97
	v_lshlrev_b32_e32 v94, 16, v95
	v_and_b32_e32 v95, 0xffff0000, v95
	v_lshlrev_b32_e32 v116, 16, v117
	v_and_b32_e32 v117, 0xffff0000, v117
	v_cvt_pk_f32_fp8_e32 v[112:113], v107
	v_cvt_pk_f32_fp8_e32 v[136:137], v109
	v_cvt_pk_f32_fp8_sdwa v[138:139], v109 src0_sel:WORD_1
	v_cvt_pk_f32_fp8_e32 v[144:145], v146
	v_cvt_pk_f32_fp8_sdwa v[146:147], v146 src0_sel:WORD_1
	v_cvt_pk_f32_fp8_sdwa v[114:115], v107 src0_sel:WORD_1
	v_cvt_pk_f32_fp8_e32 v[140:141], v111
	v_cvt_pk_f32_fp8_sdwa v[142:143], v111 src0_sel:WORD_1
	v_cvt_pk_f32_fp8_e32 v[152:153], v154
	v_cvt_pk_f32_fp8_sdwa v[154:155], v154 src0_sel:WORD_1
	v_cvt_pk_f32_fp8_e32 v[160:161], v162
	v_cvt_pk_f32_fp8_sdwa v[162:163], v162 src0_sel:WORD_1
	v_cvt_pk_f32_fp8_e32 v[168:169], v170
	v_cvt_pk_f32_fp8_sdwa v[170:171], v170 src0_sel:WORD_1
	v_cvt_pk_f32_fp8_e32 v[176:177], v178
	v_cvt_pk_f32_fp8_sdwa v[178:179], v178 src0_sel:WORD_1
	v_cvt_pk_f32_fp8_e32 v[184:185], v186
	v_cvt_pk_f32_fp8_sdwa v[186:187], v186 src0_sel:WORD_1
	v_cvt_pk_f32_fp8_e32 v[192:193], v194
	v_cvt_pk_f32_fp8_sdwa v[194:195], v194 src0_sel:WORD_1
	v_cvt_pk_f32_fp8_e32 v[148:149], v150
	v_cvt_pk_f32_fp8_sdwa v[150:151], v150 src0_sel:WORD_1
	v_cvt_pk_f32_fp8_e32 v[156:157], v158
	v_cvt_pk_f32_fp8_e32 v[172:173], v174
	v_cvt_pk_f32_fp8_e32 v[188:189], v190
	v_cvt_pk_f32_fp8_sdwa v[158:159], v158 src0_sel:WORD_1
	v_cvt_pk_f32_fp8_e32 v[164:165], v166
	v_cvt_pk_f32_fp8_sdwa v[166:167], v166 src0_sel:WORD_1
	v_cvt_pk_f32_fp8_sdwa v[174:175], v174 src0_sel:WORD_1
	v_cvt_pk_f32_fp8_e32 v[180:181], v182
	v_cvt_pk_f32_fp8_sdwa v[182:183], v182 src0_sel:WORD_1
	v_cvt_pk_f32_fp8_sdwa v[190:191], v190 src0_sel:WORD_1
	v_pk_mul_f32 v[138:139], v[108:109], v[138:139] op_sel_hi:[0,1]
	v_pk_mul_f32 v[136:137], v[108:109], v[136:137] op_sel_hi:[0,1]
	v_pk_mul_f32 v[146:147], v[108:109], v[146:147] op_sel_hi:[0,1]
	v_pk_mul_f32 v[144:145], v[108:109], v[144:145] op_sel_hi:[0,1]
	v_pk_mul_f32 v[152:153], v[108:109], v[152:153] op_sel_hi:[0,1]
	v_pk_mul_f32 v[154:155], v[108:109], v[154:155] op_sel_hi:[0,1]
	v_pk_mul_f32 v[162:163], v[108:109], v[162:163] op_sel_hi:[0,1]
	v_pk_mul_f32 v[160:161], v[108:109], v[160:161] op_sel_hi:[0,1]
	v_pk_mul_f32 v[170:171], v[108:109], v[170:171] op_sel_hi:[0,1]
	v_pk_mul_f32 v[168:169], v[108:109], v[168:169] op_sel_hi:[0,1]
	v_pk_mul_f32 v[176:177], v[108:109], v[176:177] op_sel_hi:[0,1]
; __device__ __forceinline__ void phase12(const Args& a, unsigned char* lds_g, int lane, int wave) {
;     ...
;             const auto l0 = __builtin_amdgcn_cvt_pk_f32_fp8((int)a0, false), h0 = __builtin_amdgcn_cvt_pk_f32_fp8((int)a0, true), l1 = __builtin_amdgcn_cvt_pk_f32_fp8((int)a1, false), h1 = __builtin_amdgcn_cvt_pk_f32_fp8((int)a1, true);
;             f32x4 y; y.x = w0 * l0[0] + w1 * l1[0]; y.y = w0 * l0[1] + w1 * l1[1]; y.z = w0 * h0[0] + w1 * h1[0]; y.w = w0 * h0[1] + w1 * h1[1];
;             const unsigned long long xw = xr[64 * j];
;             v[j] = (f32x4){bflo((unsigned)xw), bfhi((unsigned)xw), bflo((unsigned)(xw >> 32)), bfhi((unsigned)(xw >> 32))} + g2 * y;
;             s += (v[j].x * v[j].x + v[j].y * v[j].y) + (v[j].z * v[j].z + v[j].w * v[j].w);
;         }
	v_pk_mul_f32 v[178:179], v[108:109], v[178:179] op_sel_hi:[0,1]
	v_pk_mul_f32 v[186:187], v[108:109], v[186:187] op_sel_hi:[0,1]
	v_pk_mul_f32 v[184:185], v[108:109], v[184:185] op_sel_hi:[0,1]
	v_pk_mul_f32 v[194:195], v[108:109], v[194:195] op_sel_hi:[0,1]
	v_pk_mul_f32 v[108:109], v[108:109], v[192:193] op_sel_hi:[0,1]
	v_pk_fma_f32 v[112:113], v[110:111], v[112:113], v[136:137] op_sel_hi:[0,1,1]
	v_pk_fma_f32 v[114:115], v[110:111], v[114:115], v[138:139] op_sel_hi:[0,1,1]
	v_pk_fma_f32 v[136:137], v[110:111], v[140:141], v[144:145] op_sel_hi:[0,1,1]
	v_pk_fma_f32 v[138:139], v[110:111], v[142:143], v[146:147] op_sel_hi:[0,1,1]
	v_pk_fma_f32 v[140:141], v[110:111], v[150:151], v[154:155] op_sel_hi:[0,1,1]
	v_pk_fma_f32 v[142:143], v[110:111], v[148:149], v[152:153] op_sel_hi:[0,1,1]
	v_pk_fma_f32 v[144:145], v[110:111], v[156:157], v[160:161] op_sel_hi:[0,1,1]
	v_pk_fma_f32 v[154:155], v[110:111], v[172:173], v[176:177] op_sel_hi:[0,1,1]
	v_pk_fma_f32 v[108:109], v[110:111], v[188:189], v[108:109] op_sel_hi:[0,1,1]
	v_pk_fma_f32 v[86:87], v[10:11], v[114:115], v[86:87]
	v_pk_fma_f32 v[112:113], v[8:9], v[112:113], v[120:121]
	v_pk_fma_f32 v[88:89], v[14:15], v[138:139], v[88:89]
	v_pk_fma_f32 v[114:115], v[12:13], v[136:137], v[122:123]
	v_pk_fma_f32 v[146:147], v[110:111], v[158:159], v[162:163] op_sel_hi:[0,1,1]
	v_pk_fma_f32 v[148:149], v[110:111], v[164:165], v[168:169] op_sel_hi:[0,1,1]
	v_pk_fma_f32 v[150:151], v[110:111], v[166:167], v[170:171] op_sel_hi:[0,1,1]
	v_pk_fma_f32 v[152:153], v[110:111], v[174:175], v[178:179] op_sel_hi:[0,1,1]
	v_pk_fma_f32 v[156:157], v[110:111], v[180:181], v[184:185] op_sel_hi:[0,1,1]
	v_pk_fma_f32 v[158:159], v[110:111], v[182:183], v[186:187] op_sel_hi:[0,1,1]
	v_pk_fma_f32 v[110:111], v[110:111], v[190:191], v[194:195] op_sel_hi:[0,1,1]
	v_pk_fma_f32 v[120:121], v[20:21], v[142:143], v[124:125]
	v_pk_fma_f32 v[90:91], v[22:23], v[140:141], v[90:91]
	v_pk_fma_f32 v[122:123], v[28:29], v[144:145], v[126:127]
	v_pk_fma_f32 v[126:127], v[44:45], v[154:155], v[130:131]
	v_pk_fma_f32 v[108:109], v[60:61], v[108:109], v[134:135]
	v_mov_b32_e32 v130, v113
	v_mov_b32_e32 v131, v115
	v_mov_b32_e32 v134, v87
	v_mov_b32_e32 v135, v89
	v_pk_fma_f32 v[124:125], v[36:37], v[148:149], v[128:129]
	v_pk_fma_f32 v[128:129], v[52:53], v[156:157], v[132:133]
	v_pk_fma_f32 v[110:111], v[62:63], v[110:111], v[118:119]
	v_mov_b32_e32 v118, v112
	v_mov_b32_e32 v119, v114
	v_mov_b32_e32 v132, v86
	v_mov_b32_e32 v133, v88
	v_pk_mul_f32 v[136:137], v[90:91], v[90:91]
	v_pk_mul_f32 v[138:139], v[120:121], v[120:121]
	v_pk_mul_f32 v[130:131], v[130:131], v[130:131]
	v_pk_mul_f32 v[134:135], v[134:135], v[134:135]
	v_pk_fma_f32 v[92:93], v[30:31], v[146:147], v[92:93]
	v_pk_fma_f32 v[96:97], v[46:47], v[152:153], v[96:97]
	v_pk_mov_b32 v[152:153], v[138:139], v[136:137] op_sel:[1,0]
	v_mov_b32_e32 v139, v137
	v_pk_fma_f32 v[118:119], v[118:119], v[118:119], v[130:131]
	v_pk_fma_f32 v[130:131], v[132:133], v[132:133], v[134:135]
	v_pk_fma_f32 v[94:95], v[38:39], v[150:151], v[94:95]
	v_mul_f32_e32 v140, v123, v123
	v_mul_f32_e32 v142, v93, v93
	v_pk_add_f32 v[132:133], v[152:153], v[138:139]
	v_pk_add_f32 v[118:119], v[118:119], v[130:131]
	v_mul_f32_e32 v107, v124, v124
	v_mul_f32_e32 v151, v125, v125
	v_mul_f32_e32 v154, v94, v94
	v_mul_f32_e32 v155, v95, v95
	v_pk_fma_f32 v[136:137], v[122:123], v[122:123], v[140:141] op_sel_hi:[1,1,0]
	v_pk_fma_f32 v[140:141], v[92:93], v[92:93], v[142:143] op_sel_hi:[1,1,0]
	v_pk_add_f32 v[130:131], v[132:133], v[132:133] op_sel:[0,1] op_sel_hi:[1,0]
	v_pk_add_f32 v[118:119], v[118:119], v[118:119] op_sel:[0,1] op_sel_hi:[1,0]
	v_pk_mul_f32 v[144:145], v[96:97], v[96:97]
	v_pk_mul_f32 v[146:147], v[126:127], v[126:127]
	v_mov_b32_e32 v137, v154
	v_mov_b32_e32 v141, v155
	v_mov_b32_e32 v131, v151
	v_mov_b32_e32 v119, v107
	v_pk_fma_f32 v[116:117], v[54:55], v[158:159], v[116:117]
	v_pk_mov_b32 v[142:143], v[146:147], v[144:145] op_sel:[1,0]
	v_mov_b32_e32 v147, v145
	v_pk_add_f32 v[132:133], v[136:137], v[140:141]
	v_pk_add_f32 v[118:119], v[118:119], v[130:131]
	v_mul_f32_e32 v148, v129, v129
	v_mul_f32_e32 v150, v117, v117
	v_pk_add_f32 v[134:135], v[142:143], v[146:147]
	v_pk_add_f32 v[118:119], v[118:119], v[132:133]
	v_mul_f32_e32 v156, v108, v108
	v_mul_f32_e32 v157, v109, v109
	v_mul_f32_e32 v158, v110, v110
	v_mul_f32_e32 v159, v111, v111
	v_pk_fma_f32 v[144:145], v[128:129], v[128:129], v[148:149] op_sel_hi:[1,1,0]
	v_pk_fma_f32 v[148:149], v[116:117], v[116:117], v[150:151] op_sel_hi:[1,1,0]
	v_pk_add_f32 v[134:135], v[134:135], v[134:135] op_sel:[0,1] op_sel_hi:[1,0]
	v_pk_add_f32 v[118:119], v[118:119], v[118:119] op_sel:[0,1] op_sel_hi:[1,0]
	v_mov_b32_e32 v145, v158
	v_mov_b32_e32 v149, v159
	v_mov_b32_e32 v135, v157
	v_mov_b32_e32 v119, v156
	v_pk_add_f32 v[136:137], v[144:145], v[148:149]
	v_pk_add_f32 v[118:119], v[118:119], v[134:135]
	s_nop 0
	v_pk_add_f32 v[118:119], v[118:119], v[136:137]
	s_nop 0
	v_add_f32_e32 v107, v118, v119
	ds_bpermute_b32 v118, v99, v107
	s_waitcnt lgkmcnt(0)
	v_add_f32_e32 v107, v107, v118
	ds_bpermute_b32 v118, v100, v107
	s_waitcnt lgkmcnt(0)
	v_add_f32_e32 v107, v107, v118
	ds_bpermute_b32 v118, v101, v107
	s_waitcnt lgkmcnt(0)
	v_add_f32_e32 v107, v107, v118
	ds_bpermute_b32 v118, v102, v107
	s_waitcnt lgkmcnt(0)
	v_add_f32_e32 v107, v107, v118
	ds_bpermute_b32 v118, v103, v107
	s_waitcnt lgkmcnt(0)
	v_add_f32_e32 v107, v107, v118
	ds_bpermute_b32 v118, v104, v107
	s_waitcnt lgkmcnt(0)
; __device__ __forceinline__ void phase12(const Args& a, unsigned char* lds_g, int lane, int wave) {
;     ...
;         const int4 q0 = ASG[2 * t], q1 = ASG[2 * t + 1];
;         const float w0 = __int_as_float(q0.z), w1 = __int_as_float(q1.z);
;         const unsigned long long* xr = (const unsigned long long*)(X1 + (size_t)t * D) + lane;
;         const unsigned* y0 = (const unsigned*)(Y2 + (size_t)(256 * cum[q0.x] + q0.y) * D) + lane; const unsigned* y1 = (const unsigned*)(Y2 + (size_t)(256 * cum[q1.x] + q1.y) * D) + lane;
;         f32x4 v[8]; float s = 0.f;
; #pragma unroll
;         for (int j = 0; j < 8; ++j) {
;             const int c = 4 * lane + 256 * j;
;             const f32x4 g2 = g2v[j]; (void)c;
;             const unsigned a0 = y0[64 * j], a1 = y1[64 * j];
;             const auto l0 = __builtin_amdgcn_cvt_pk_f32_fp8((int)a0, false), h0 = __builtin_amdgcn_cvt_pk_f32_fp8((int)a0, true), l1 = __builtin_amdgcn_cvt_pk_f32_fp8((int)a1, false), h1 = __builtin_amdgcn_cvt_pk_f32_fp8((int)a1, true);
;             f32x4 y; y.x = w0 * l0[0] + w1 * l1[0]; y.y = w0 * l0[1] + w1 * l1[1]; y.z = w0 * h0[0] + w1 * h1[0]; y.w = w0 * h0[1] + w1 * h1[1];
;             const unsigned long long xw = xr[64 * j];
;     ...
;         }
;         const float rstd = 1.f / sqrtf(wave_sum(s) * (1.f / D) + EPS);
;         f32x4* o = (f32x4*)(a.out + (size_t)t * D) + lane;
; #pragma unroll
;         for (int j = 0; j < 8; ++j) o[64 * j] = v[j] * rstd * fgv[j];
	v_add_f32_e32 v107, v107, v118
	v_fmamk_f32 v107, v107, 0x3a000000, v105
	v_mul_f32_e32 v118, 0x4f800000, v107
	v_cmp_gt_f32_e32 vcc, s11, v107
	s_nop 1
	v_cndmask_b32_e32 v107, v107, v118, vcc
	v_sqrt_f32_e32 v118, v107
	s_nop 0
	v_add_u32_e32 v119, -1, v118
	v_add_u32_e32 v130, 1, v118
	v_fma_f32 v131, -v119, v118, v107
	v_fma_f32 v132, -v130, v118, v107
	v_cmp_ge_f32_e64 s[0:1], 0, v131
	s_nop 1
	v_cndmask_b32_e64 v118, v118, v119, s[0:1]
	v_cmp_lt_f32_e64 s[0:1], 0, v132
	s_nop 1
	v_cndmask_b32_e64 v118, v118, v130, s[0:1]
	v_mul_f32_e32 v119, 0x37800000, v118
	v_cndmask_b32_e32 v118, v118, v119, vcc
	v_cmp_class_f32_e32 vcc, v107, v106
	s_nop 1
	v_cndmask_b32_e32 v107, v118, v107, vcc
	v_div_scale_f32 v118, s[0:1], v107, v107, 1.0
	v_rcp_f32_e32 v130, v118
	v_div_scale_f32 v119, vcc, 1.0, v107, 1.0
	v_fma_f32 v131, -v118, v130, 1.0
	v_fmac_f32_e32 v130, v131, v130
	v_mul_f32_e32 v131, v119, v130
	v_fma_f32 v132, -v118, v131, v119
	v_fmac_f32_e32 v131, v132, v130
	v_fma_f32 v118, -v118, v131, v119
	v_div_fmas_f32 v118, v118, v130, v131
	v_div_fixup_f32 v118, v118, v107, 1.0
	v_pk_mul_f32 v[112:113], v[112:113], v[118:119] op_sel_hi:[1,0]
	v_pk_mul_f32 v[86:87], v[86:87], v[118:119] op_sel_hi:[1,0]
	v_pk_mul_f32 v[114:115], v[114:115], v[118:119] op_sel_hi:[1,0]
	v_pk_mul_f32 v[130:131], v[88:89], v[118:119] op_sel_hi:[1,0]
	v_pk_mul_f32 v[120:121], v[120:121], v[118:119] op_sel_hi:[1,0]
	v_pk_mul_f32 v[132:133], v[90:91], v[118:119] op_sel_hi:[1,0]
	v_pk_mul_f32 v[122:123], v[122:123], v[118:119] op_sel_hi:[1,0]
	v_pk_mul_f32 v[134:135], v[92:93], v[118:119] op_sel_hi:[1,0]
	v_pk_mul_f32 v[124:125], v[124:125], v[118:119] op_sel_hi:[1,0]
	v_pk_mul_f32 v[136:137], v[94:95], v[118:119] op_sel_hi:[1,0]
	v_pk_mul_f32 v[126:127], v[126:127], v[118:119] op_sel_hi:[1,0]
	v_pk_mul_f32 v[138:139], v[96:97], v[118:119] op_sel_hi:[1,0]
	v_pk_mul_f32 v[128:129], v[128:129], v[118:119] op_sel_hi:[1,0]
	v_pk_mul_f32 v[140:141], v[116:117], v[118:119] op_sel_hi:[1,0]
	v_pk_mul_f32 v[142:143], v[108:109], v[118:119] op_sel_hi:[1,0]
	v_pk_mul_f32 v[144:145], v[110:111], v[118:119] op_sel_hi:[1,0]
	v_pk_mul_f32 v[88:89], v[2:3], v[86:87]
	v_pk_mul_f32 v[86:87], v[0:1], v[112:113]
	v_pk_mul_f32 v[92:93], v[6:7], v[130:131]
	v_pk_mul_f32 v[90:91], v[4:5], v[114:115]
	v_pk_mul_f32 v[96:97], v[18:19], v[132:133]
	v_pk_mul_f32 v[94:95], v[16:17], v[120:121]
	v_pk_mul_f32 v[110:111], v[26:27], v[134:135]
	v_pk_mul_f32 v[108:109], v[24:25], v[122:123]
	v_pk_mul_f32 v[114:115], v[34:35], v[136:137]
	v_pk_mul_f32 v[112:113], v[32:33], v[124:125]
	v_pk_mul_f32 v[118:119], v[42:43], v[138:139]
	v_pk_mul_f32 v[116:117], v[40:41], v[126:127]
	v_pk_mul_f32 v[122:123], v[50:51], v[140:141]
	v_pk_mul_f32 v[120:121], v[48:49], v[128:129]
	v_pk_mul_f32 v[126:127], v[58:59], v[144:145]
	v_pk_mul_f32 v[124:125], v[56:57], v[142:143]
	global_store_dwordx4 v[84:85], v[86:89], off offset:-4096 sc0 sc1
	global_store_dwordx4 v[84:85], v[90:93], off offset:-3072 sc0 sc1
	global_store_dwordx4 v[84:85], v[94:97], off offset:-2048 sc0 sc1
	global_store_dwordx4 v[84:85], v[108:111], off offset:-1024 sc0 sc1
	global_store_dwordx4 v[84:85], v[112:115], off sc0 sc1
	global_store_dwordx4 v[84:85], v[116:119], off offset:1024 sc0 sc1
	global_store_dwordx4 v[84:85], v[120:123], off offset:2048 sc0 sc1
	global_store_dwordx4 v[84:85], v[124:127], off offset:3072 sc0 sc1
	v_lshl_add_u64 v[84:85], v[84:85], 0, s[18:19]
	s_waitcnt vmcnt(8)
	v_mov_b64_e32 v[86:87], v[196:197]
	v_mov_b64_e32 v[88:89], v[198:199]
	v_mov_b64_e32 v[90:91], v[200:201]
	v_mov_b64_e32 v[92:93], v[202:203]
	v_mov_b64_e32 v[94:95], v[204:205]
	v_mov_b64_e32 v[96:97], v[206:207]
	v_mov_b64_e32 v[116:117], v[208:209]
	v_mov_b64_e32 v[118:119], v[210:211]
	v_mov_b32_e32 v107, v212
	v_mov_b32_e32 v109, v213
	v_mov_b32_e32 v111, v214
	v_mov_b32_e32 v146, v215
	v_mov_b32_e32 v150, v216
	v_mov_b32_e32 v154, v217
	v_mov_b32_e32 v158, v218
	v_mov_b32_e32 v162, v219
	v_mov_b32_e32 v166, v220
	v_mov_b32_e32 v170, v221
	v_mov_b32_e32 v174, v222
	v_mov_b32_e32 v178, v223
	v_mov_b32_e32 v182, v224
	v_mov_b32_e32 v186, v225
	v_mov_b32_e32 v190, v226
	v_mov_b32_e32 v194, v227
	global_load_dwordx2 v[196:197], v[82:83], off offset:-2048
	global_load_dwordx2 v[198:199], v[82:83], off offset:-1536
	global_load_dwordx2 v[200:201], v[82:83], off offset:-1024
	global_load_dwordx2 v[202:203], v[82:83], off offset:-512
	global_load_dwordx2 v[204:205], v[82:83], off
	global_load_dwordx2 v[206:207], v[82:83], off offset:512
	global_load_dwordx2 v[208:209], v[82:83], off offset:1024
	global_load_dwordx2 v[210:211], v[82:83], off offset:1536
	v_lshl_add_u64 v[82:83], v[82:83], 0, s[12:13]
	v_add_co_u32_e32 v244, vcc, v68, v240
	s_nop 1
	v_addc_co_u32_e32 v245, vcc, 0, v69, vcc
	v_add_co_u32_e32 v246, vcc, v68, v241
	s_nop 1
	v_addc_co_u32_e32 v247, vcc, 0, v69, vcc
	global_load_dword v212, v[244:245], off
	global_load_dword v213, v[246:247], off
	global_load_dword v214, v[244:245], off offset:256
	global_load_dword v215, v[246:247], off offset:256
	global_load_dword v216, v[244:245], off offset:512
	global_load_dword v217, v[246:247], off offset:512
	global_load_dword v218, v[244:245], off offset:768
	global_load_dword v219, v[246:247], off offset:768
	global_load_dword v220, v[244:245], off offset:1024
	global_load_dword v221, v[246:247], off offset:1024
	global_load_dword v222, v[244:245], off offset:1280
	global_load_dword v223, v[246:247], off offset:1280
	global_load_dword v224, v[244:245], off offset:1536
	global_load_dword v225, v[246:247], off offset:1536
	global_load_dword v226, v[244:245], off offset:1792
	global_load_dword v227, v[246:247], off offset:1792
; __device__ __forceinline__ void phase12(const Args& a, unsigned char* lds_g, int lane, int wave) {
;     ...
;         for (int j = 0; j < 8; ++j) {
;             const int c = 4 * lane + 256 * j;
;             const f32x4 g2 = g2v[j]; (void)c;
;             const unsigned a0 = y0[64 * j], a1 = y1[64 * j];
;             const auto l0 = __builtin_amdgcn_cvt_pk_f32_fp8((int)a0, false), h0 = __builtin_amdgcn_cvt_pk_f32_fp8((int)a0, true), l1 = __builtin_amdgcn_cvt_pk_f32_fp8((int)a1, false), h1 = __builtin_amdgcn_cvt_pk_f32_fp8((int)a1, true);
;             f32x4 y; y.x = w0 * l0[0] + w1 * l1[0]; y.y = w0 * l0[1] + w1 * l1[1]; y.z = w0 * h0[0] + w1 * h1[0]; y.w = w0 * h0[1] + w1 * h1[1];
;             const unsigned long long xw = xr[64 * j];
;             v[j] = (f32x4){bflo((unsigned)xw), bfhi((unsigned)xw), bflo((unsigned)(xw >> 32)), bfhi((unsigned)(xw >> 32))} + g2 * y;
	v_mov_b32_e32 v110, v238
	v_mov_b32_e32 v108, v239
	v_lshlrev_b32_e32 v120, 16, v86
	v_and_b32_e32 v121, 0xffff0000, v86
	v_lshlrev_b32_e32 v86, 16, v87
	v_and_b32_e32 v87, 0xffff0000, v87
	v_lshlrev_b32_e32 v122, 16, v88
	v_and_b32_e32 v123, 0xffff0000, v88
	v_lshlrev_b32_e32 v88, 16, v89
	v_and_b32_e32 v89, 0xffff0000, v89
	v_lshlrev_b32_e32 v124, 16, v90
	v_and_b32_e32 v125, 0xffff0000, v90
	v_lshlrev_b32_e32 v90, 16, v91
	v_and_b32_e32 v91, 0xffff0000, v91
	v_lshlrev_b32_e32 v126, 16, v92
	v_and_b32_e32 v127, 0xffff0000, v92
	v_lshlrev_b32_e32 v130, 16, v96
	v_and_b32_e32 v131, 0xffff0000, v96
	v_lshlrev_b32_e32 v134, 16, v118
	v_and_b32_e32 v135, 0xffff0000, v118
	v_lshlrev_b32_e32 v128, 16, v94
	v_and_b32_e32 v129, 0xffff0000, v94
	v_lshlrev_b32_e32 v132, 16, v116
	v_and_b32_e32 v133, 0xffff0000, v116
	v_lshlrev_b32_e32 v118, 16, v119
	v_and_b32_e32 v119, 0xffff0000, v119
	v_lshlrev_b32_e32 v92, 16, v93
	v_and_b32_e32 v93, 0xffff0000, v93
	v_lshlrev_b32_e32 v96, 16, v97
	v_and_b32_e32 v97, 0xffff0000, v97
	v_lshlrev_b32_e32 v94, 16, v95
	v_and_b32_e32 v95, 0xffff0000, v95
	v_lshlrev_b32_e32 v116, 16, v117
	v_and_b32_e32 v117, 0xffff0000, v117
	v_cvt_pk_f32_fp8_e32 v[112:113], v107
	v_cvt_pk_f32_fp8_e32 v[136:137], v109
	v_cvt_pk_f32_fp8_sdwa v[138:139], v109 src0_sel:WORD_1
	v_cvt_pk_f32_fp8_e32 v[144:145], v146
	v_cvt_pk_f32_fp8_sdwa v[146:147], v146 src0_sel:WORD_1
	v_cvt_pk_f32_fp8_sdwa v[114:115], v107 src0_sel:WORD_1
	v_cvt_pk_f32_fp8_e32 v[140:141], v111
	v_cvt_pk_f32_fp8_sdwa v[142:143], v111 src0_sel:WORD_1
	v_cvt_pk_f32_fp8_e32 v[152:153], v154
	v_cvt_pk_f32_fp8_sdwa v[154:155], v154 src0_sel:WORD_1
	v_cvt_pk_f32_fp8_e32 v[160:161], v162
	v_cvt_pk_f32_fp8_sdwa v[162:163], v162 src0_sel:WORD_1
	v_cvt_pk_f32_fp8_e32 v[168:169], v170
	v_cvt_pk_f32_fp8_sdwa v[170:171], v170 src0_sel:WORD_1
	v_cvt_pk_f32_fp8_e32 v[176:177], v178
	v_cvt_pk_f32_fp8_sdwa v[178:179], v178 src0_sel:WORD_1
	v_cvt_pk_f32_fp8_e32 v[184:185], v186
	v_cvt_pk_f32_fp8_sdwa v[186:187], v186 src0_sel:WORD_1
	v_cvt_pk_f32_fp8_e32 v[192:193], v194
	v_cvt_pk_f32_fp8_sdwa v[194:195], v194 src0_sel:WORD_1
	v_cvt_pk_f32_fp8_e32 v[148:149], v150
	v_cvt_pk_f32_fp8_sdwa v[150:151], v150 src0_sel:WORD_1
	v_cvt_pk_f32_fp8_e32 v[156:157], v158
	v_cvt_pk_f32_fp8_e32 v[172:173], v174
	v_cvt_pk_f32_fp8_e32 v[188:189], v190
	v_cvt_pk_f32_fp8_sdwa v[158:159], v158 src0_sel:WORD_1
	v_cvt_pk_f32_fp8_e32 v[164:165], v166
	v_cvt_pk_f32_fp8_sdwa v[166:167], v166 src0_sel:WORD_1
	v_cvt_pk_f32_fp8_sdwa v[174:175], v174 src0_sel:WORD_1
	v_cvt_pk_f32_fp8_e32 v[180:181], v182
	v_cvt_pk_f32_fp8_sdwa v[182:183], v182 src0_sel:WORD_1
	v_cvt_pk_f32_fp8_sdwa v[190:191], v190 src0_sel:WORD_1
	v_pk_mul_f32 v[138:139], v[108:109], v[138:139] op_sel_hi:[0,1]
	v_pk_mul_f32 v[136:137], v[108:109], v[136:137] op_sel_hi:[0,1]
	v_pk_mul_f32 v[146:147], v[108:109], v[146:147] op_sel_hi:[0,1]
	v_pk_mul_f32 v[144:145], v[108:109], v[144:145] op_sel_hi:[0,1]
	v_pk_mul_f32 v[152:153], v[108:109], v[152:153] op_sel_hi:[0,1]
	v_pk_mul_f32 v[154:155], v[108:109], v[154:155] op_sel_hi:[0,1]
	v_pk_mul_f32 v[162:163], v[108:109], v[162:163] op_sel_hi:[0,1]
	v_pk_mul_f32 v[160:161], v[108:109], v[160:161] op_sel_hi:[0,1]
	v_pk_mul_f32 v[170:171], v[108:109], v[170:171] op_sel_hi:[0,1]
	v_pk_mul_f32 v[168:169], v[108:109], v[168:169] op_sel_hi:[0,1]
	v_pk_mul_f32 v[176:177], v[108:109], v[176:177] op_sel_hi:[0,1]
	v_pk_mul_f32 v[178:179], v[108:109], v[178:179] op_sel_hi:[0,1]
	v_pk_mul_f32 v[186:187], v[108:109], v[186:187] op_sel_hi:[0,1]
	v_pk_mul_f32 v[184:185], v[108:109], v[184:185] op_sel_hi:[0,1]
	v_pk_mul_f32 v[194:195], v[108:109], v[194:195] op_sel_hi:[0,1]
	v_pk_mul_f32 v[108:109], v[108:109], v[192:193] op_sel_hi:[0,1]
	v_pk_fma_f32 v[112:113], v[110:111], v[112:113], v[136:137] op_sel_hi:[0,1,1]
	v_pk_fma_f32 v[114:115], v[110:111], v[114:115], v[138:139] op_sel_hi:[0,1,1]
	v_pk_fma_f32 v[136:137], v[110:111], v[140:141], v[144:145] op_sel_hi:[0,1,1]
	v_pk_fma_f32 v[138:139], v[110:111], v[142:143], v[146:147] op_sel_hi:[0,1,1]
	v_pk_fma_f32 v[140:141], v[110:111], v[150:151], v[154:155] op_sel_hi:[0,1,1]
	v_pk_fma_f32 v[142:143], v[110:111], v[148:149], v[152:153] op_sel_hi:[0,1,1]
	v_pk_fma_f32 v[144:145], v[110:111], v[156:157], v[160:161] op_sel_hi:[0,1,1]
	v_pk_fma_f32 v[154:155], v[110:111], v[172:173], v[176:177] op_sel_hi:[0,1,1]
	v_pk_fma_f32 v[108:109], v[110:111], v[188:189], v[108:109] op_sel_hi:[0,1,1]
	v_pk_fma_f32 v[86:87], v[10:11], v[114:115], v[86:87]
	v_pk_fma_f32 v[112:113], v[8:9], v[112:113], v[120:121]
	v_pk_fma_f32 v[88:89], v[14:15], v[138:139], v[88:89]
	v_pk_fma_f32 v[114:115], v[12:13], v[136:137], v[122:123]
	v_pk_fma_f32 v[146:147], v[110:111], v[158:159], v[162:163] op_sel_hi:[0,1,1]
	v_pk_fma_f32 v[148:149], v[110:111], v[164:165], v[168:169] op_sel_hi:[0,1,1]
	v_pk_fma_f32 v[150:151], v[110:111], v[166:167], v[170:171] op_sel_hi:[0,1,1]
	v_pk_fma_f32 v[152:153], v[110:111], v[174:175], v[178:179] op_sel_hi:[0,1,1]
	v_pk_fma_f32 v[156:157], v[110:111], v[180:181], v[184:185] op_sel_hi:[0,1,1]
	v_pk_fma_f32 v[158:159], v[110:111], v[182:183], v[186:187] op_sel_hi:[0,1,1]
	v_pk_fma_f32 v[110:111], v[110:111], v[190:191], v[194:195] op_sel_hi:[0,1,1]
	v_pk_fma_f32 v[120:121], v[20:21], v[142:143], v[124:125]
	v_pk_fma_f32 v[90:91], v[22:23], v[140:141], v[90:91]
	v_pk_fma_f32 v[122:123], v[28:29], v[144:145], v[126:127]
	v_pk_fma_f32 v[126:127], v[44:45], v[154:155], v[130:131]
	v_pk_fma_f32 v[108:109], v[60:61], v[108:109], v[134:135]
	v_mov_b32_e32 v130, v113
	v_mov_b32_e32 v131, v115
	v_mov_b32_e32 v134, v87
	v_mov_b32_e32 v135, v89
; __device__ __forceinline__ void phase12(const Args& a, unsigned char* lds_g, int lane, int wave) {
;     ...
;             const auto l0 = __builtin_amdgcn_cvt_pk_f32_fp8((int)a0, false), h0 = __builtin_amdgcn_cvt_pk_f32_fp8((int)a0, true), l1 = __builtin_amdgcn_cvt_pk_f32_fp8((int)a1, false), h1 = __builtin_amdgcn_cvt_pk_f32_fp8((int)a1, true);
;             f32x4 y; y.x = w0 * l0[0] + w1 * l1[0]; y.y = w0 * l0[1] + w1 * l1[1]; y.z = w0 * h0[0] + w1 * h1[0]; y.w = w0 * h0[1] + w1 * h1[1];
;             const unsigned long long xw = xr[64 * j];
;             v[j] = (f32x4){bflo((unsigned)xw), bfhi((unsigned)xw), bflo((unsigned)(xw >> 32)), bfhi((unsigned)(xw >> 32))} + g2 * y;
;             s += (v[j].x * v[j].x + v[j].y * v[j].y) + (v[j].z * v[j].z + v[j].w * v[j].w);
;         }
;         const float rstd = 1.f / sqrtf(wave_sum(s) * (1.f / D) + EPS);
;         f32x4* o = (f32x4*)(a.out + (size_t)t * D) + lane;
; #pragma unroll
;         for (int j = 0; j < 8; ++j) o[64 * j] = v[j] * rstd * fgv[j];
	v_pk_fma_f32 v[124:125], v[36:37], v[148:149], v[128:129]
	v_pk_fma_f32 v[128:129], v[52:53], v[156:157], v[132:133]
	v_pk_fma_f32 v[110:111], v[62:63], v[110:111], v[118:119]
	v_mov_b32_e32 v118, v112
	v_mov_b32_e32 v119, v114
	v_mov_b32_e32 v132, v86
	v_mov_b32_e32 v133, v88
	v_pk_mul_f32 v[136:137], v[90:91], v[90:91]
	v_pk_mul_f32 v[138:139], v[120:121], v[120:121]
	v_pk_mul_f32 v[130:131], v[130:131], v[130:131]
	v_pk_mul_f32 v[134:135], v[134:135], v[134:135]
	v_pk_fma_f32 v[92:93], v[30:31], v[146:147], v[92:93]
	v_pk_fma_f32 v[96:97], v[46:47], v[152:153], v[96:97]
	v_pk_mov_b32 v[152:153], v[138:139], v[136:137] op_sel:[1,0]
	v_mov_b32_e32 v139, v137
	v_pk_fma_f32 v[118:119], v[118:119], v[118:119], v[130:131]
	v_pk_fma_f32 v[130:131], v[132:133], v[132:133], v[134:135]
	v_pk_fma_f32 v[94:95], v[38:39], v[150:151], v[94:95]
	v_mul_f32_e32 v140, v123, v123
	v_mul_f32_e32 v142, v93, v93
	v_pk_add_f32 v[132:133], v[152:153], v[138:139]
	v_pk_add_f32 v[118:119], v[118:119], v[130:131]
	v_mul_f32_e32 v107, v124, v124
	v_mul_f32_e32 v151, v125, v125
	v_mul_f32_e32 v154, v94, v94
	v_mul_f32_e32 v155, v95, v95
	v_pk_fma_f32 v[136:137], v[122:123], v[122:123], v[140:141] op_sel_hi:[1,1,0]
	v_pk_fma_f32 v[140:141], v[92:93], v[92:93], v[142:143] op_sel_hi:[1,1,0]
	v_pk_add_f32 v[130:131], v[132:133], v[132:133] op_sel:[0,1] op_sel_hi:[1,0]
	v_pk_add_f32 v[118:119], v[118:119], v[118:119] op_sel:[0,1] op_sel_hi:[1,0]
	v_pk_mul_f32 v[144:145], v[96:97], v[96:97]
	v_pk_mul_f32 v[146:147], v[126:127], v[126:127]
	v_mov_b32_e32 v137, v154
	v_mov_b32_e32 v141, v155
	v_mov_b32_e32 v131, v151
	v_mov_b32_e32 v119, v107
	v_pk_fma_f32 v[116:117], v[54:55], v[158:159], v[116:117]
	v_pk_mov_b32 v[142:143], v[146:147], v[144:145] op_sel:[1,0]
	v_mov_b32_e32 v147, v145
	v_pk_add_f32 v[132:133], v[136:137], v[140:141]
	v_pk_add_f32 v[118:119], v[118:119], v[130:131]
	v_mul_f32_e32 v148, v129, v129
	v_mul_f32_e32 v150, v117, v117
	v_pk_add_f32 v[134:135], v[142:143], v[146:147]
	v_pk_add_f32 v[118:119], v[118:119], v[132:133]
	v_mul_f32_e32 v156, v108, v108
	v_mul_f32_e32 v157, v109, v109
	v_mul_f32_e32 v158, v110, v110
	v_mul_f32_e32 v159, v111, v111
	v_pk_fma_f32 v[144:145], v[128:129], v[128:129], v[148:149] op_sel_hi:[1,1,0]
	v_pk_fma_f32 v[148:149], v[116:117], v[116:117], v[150:151] op_sel_hi:[1,1,0]
	v_pk_add_f32 v[134:135], v[134:135], v[134:135] op_sel:[0,1] op_sel_hi:[1,0]
	v_pk_add_f32 v[118:119], v[118:119], v[118:119] op_sel:[0,1] op_sel_hi:[1,0]
	v_mov_b32_e32 v145, v158
	v_mov_b32_e32 v149, v159
	v_mov_b32_e32 v135, v157
	v_mov_b32_e32 v119, v156
	v_pk_add_f32 v[136:137], v[144:145], v[148:149]
	v_pk_add_f32 v[118:119], v[118:119], v[134:135]
	s_nop 0
	v_pk_add_f32 v[118:119], v[118:119], v[136:137]
	s_nop 0
	v_add_f32_e32 v107, v118, v119
	ds_bpermute_b32 v118, v99, v107
	s_waitcnt lgkmcnt(0)
	v_add_f32_e32 v107, v107, v118
	ds_bpermute_b32 v118, v100, v107
	s_waitcnt lgkmcnt(0)
	v_add_f32_e32 v107, v107, v118
	ds_bpermute_b32 v118, v101, v107
	s_waitcnt lgkmcnt(0)
	v_add_f32_e32 v107, v107, v118
	ds_bpermute_b32 v118, v102, v107
	s_waitcnt lgkmcnt(0)
	v_add_f32_e32 v107, v107, v118
	ds_bpermute_b32 v118, v103, v107
	s_waitcnt lgkmcnt(0)
	v_add_f32_e32 v107, v107, v118
	ds_bpermute_b32 v118, v104, v107
	s_waitcnt lgkmcnt(0)
	v_add_f32_e32 v107, v107, v118
	v_fmamk_f32 v107, v107, 0x3a000000, v105
	v_mul_f32_e32 v118, 0x4f800000, v107
	v_cmp_gt_f32_e32 vcc, s11, v107
	s_nop 1
	v_cndmask_b32_e32 v107, v107, v118, vcc
	v_sqrt_f32_e32 v118, v107
	s_nop 0
	v_add_u32_e32 v119, -1, v118
	v_add_u32_e32 v130, 1, v118
	v_fma_f32 v131, -v119, v118, v107
	v_fma_f32 v132, -v130, v118, v107
	v_cmp_ge_f32_e64 s[0:1], 0, v131
	s_nop 1
	v_cndmask_b32_e64 v118, v118, v119, s[0:1]
	v_cmp_lt_f32_e64 s[0:1], 0, v132
	s_nop 1
	v_cndmask_b32_e64 v118, v118, v130, s[0:1]
	v_mul_f32_e32 v119, 0x37800000, v118
	v_cndmask_b32_e32 v118, v118, v119, vcc
	v_cmp_class_f32_e32 vcc, v107, v106
	s_nop 1
	v_cndmask_b32_e32 v107, v118, v107, vcc
	v_div_scale_f32 v118, s[0:1], v107, v107, 1.0
	v_rcp_f32_e32 v130, v118
	v_div_scale_f32 v119, vcc, 1.0, v107, 1.0
	v_fma_f32 v131, -v118, v130, 1.0
	v_fmac_f32_e32 v130, v131, v130
	v_mul_f32_e32 v131, v119, v130
	v_fma_f32 v132, -v118, v131, v119
	v_fmac_f32_e32 v131, v132, v130
	v_fma_f32 v118, -v118, v131, v119
	v_div_fmas_f32 v118, v118, v130, v131
	v_div_fixup_f32 v118, v118, v107, 1.0
	v_pk_mul_f32 v[112:113], v[112:113], v[118:119] op_sel_hi:[1,0]
	v_pk_mul_f32 v[86:87], v[86:87], v[118:119] op_sel_hi:[1,0]
	v_pk_mul_f32 v[114:115], v[114:115], v[118:119] op_sel_hi:[1,0]
	v_pk_mul_f32 v[130:131], v[88:89], v[118:119] op_sel_hi:[1,0]
	v_pk_mul_f32 v[120:121], v[120:121], v[118:119] op_sel_hi:[1,0]
	v_pk_mul_f32 v[132:133], v[90:91], v[118:119] op_sel_hi:[1,0]
	v_pk_mul_f32 v[122:123], v[122:123], v[118:119] op_sel_hi:[1,0]
	v_pk_mul_f32 v[134:135], v[92:93], v[118:119] op_sel_hi:[1,0]
	v_pk_mul_f32 v[124:125], v[124:125], v[118:119] op_sel_hi:[1,0]
	v_pk_mul_f32 v[136:137], v[94:95], v[118:119] op_sel_hi:[1,0]
	v_pk_mul_f32 v[126:127], v[126:127], v[118:119] op_sel_hi:[1,0]
	v_pk_mul_f32 v[138:139], v[96:97], v[118:119] op_sel_hi:[1,0]
	v_pk_mul_f32 v[128:129], v[128:129], v[118:119] op_sel_hi:[1,0]
	v_pk_mul_f32 v[140:141], v[116:117], v[118:119] op_sel_hi:[1,0]
	v_pk_mul_f32 v[142:143], v[108:109], v[118:119] op_sel_hi:[1,0]
	v_pk_mul_f32 v[144:145], v[110:111], v[118:119] op_sel_hi:[1,0]
	v_pk_mul_f32 v[88:89], v[2:3], v[86:87]
	v_pk_mul_f32 v[86:87], v[0:1], v[112:113]
	v_pk_mul_f32 v[92:93], v[6:7], v[130:131]
	v_pk_mul_f32 v[90:91], v[4:5], v[114:115]
	v_pk_mul_f32 v[96:97], v[18:19], v[132:133]
	v_pk_mul_f32 v[94:95], v[16:17], v[120:121]
	v_pk_mul_f32 v[110:111], v[26:27], v[134:135]
	v_pk_mul_f32 v[108:109], v[24:25], v[122:123]
	v_pk_mul_f32 v[114:115], v[34:35], v[136:137]
	v_pk_mul_f32 v[112:113], v[32:33], v[124:125]
	v_pk_mul_f32 v[118:119], v[42:43], v[138:139]
	v_pk_mul_f32 v[116:117], v[40:41], v[126:127]
	v_pk_mul_f32 v[122:123], v[50:51], v[140:141]
	v_pk_mul_f32 v[120:121], v[48:49], v[128:129]
	v_pk_mul_f32 v[126:127], v[58:59], v[144:145]
	v_pk_mul_f32 v[124:125], v[56:57], v[142:143]
	global_store_dwordx4 v[84:85], v[86:89], off offset:-4096 sc0 sc1
	global_store_dwordx4 v[84:85], v[90:93], off offset:-3072 sc0 sc1
	global_store_dwordx4 v[84:85], v[94:97], off offset:-2048 sc0 sc1
	global_store_dwordx4 v[84:85], v[108:111], off offset:-1024 sc0 sc1
	global_store_dwordx4 v[84:85], v[112:115], off sc0 sc1
	global_store_dwordx4 v[84:85], v[116:119], off offset:1024 sc0 sc1
	global_store_dwordx4 v[84:85], v[120:123], off offset:2048 sc0 sc1
	global_store_dwordx4 v[84:85], v[124:127], off offset:3072 sc0 sc1
	v_lshl_add_u64 v[84:85], v[84:85], 0, s[18:19]
	s_waitcnt vmcnt(8)
; __device__ __forceinline__ void phase12(const Args& a, unsigned char* lds_g, int lane, int wave) {
;     ...
;         const int4 q0 = ASG[2 * t], q1 = ASG[2 * t + 1];
;         const float w0 = __int_as_float(q0.z), w1 = __int_as_float(q1.z);
;         const unsigned long long* xr = (const unsigned long long*)(X1 + (size_t)t * D) + lane;
;         const unsigned* y0 = (const unsigned*)(Y2 + (size_t)(256 * cum[q0.x] + q0.y) * D) + lane; const unsigned* y1 = (const unsigned*)(Y2 + (size_t)(256 * cum[q1.x] + q1.y) * D) + lane;
;         f32x4 v[8]; float s = 0.f;
; #pragma unroll
;         for (int j = 0; j < 8; ++j) {
;             const int c = 4 * lane + 256 * j;
;             const f32x4 g2 = g2v[j]; (void)c;
;             const unsigned a0 = y0[64 * j], a1 = y1[64 * j];
;             const auto l0 = __builtin_amdgcn_cvt_pk_f32_fp8((int)a0, false), h0 = __builtin_amdgcn_cvt_pk_f32_fp8((int)a0, true), l1 = __builtin_amdgcn_cvt_pk_f32_fp8((int)a1, false), h1 = __builtin_amdgcn_cvt_pk_f32_fp8((int)a1, true);
;             f32x4 y; y.x = w0 * l0[0] + w1 * l1[0]; y.y = w0 * l0[1] + w1 * l1[1]; y.z = w0 * h0[0] + w1 * h1[0]; y.w = w0 * h0[1] + w1 * h1[1];
;             const unsigned long long xw = xr[64 * j];
;             v[j] = (f32x4){bflo((unsigned)xw), bfhi((unsigned)xw), bflo((unsigned)(xw >> 32)), bfhi((unsigned)(xw >> 32))} + g2 * y;
	v_mov_b64_e32 v[86:87], v[196:197]
	v_mov_b64_e32 v[88:89], v[198:199]
	v_mov_b64_e32 v[90:91], v[200:201]
	v_mov_b64_e32 v[92:93], v[202:203]
	v_mov_b64_e32 v[94:95], v[204:205]
	v_mov_b64_e32 v[96:97], v[206:207]
	v_mov_b64_e32 v[116:117], v[208:209]
	v_mov_b64_e32 v[118:119], v[210:211]
	v_mov_b32_e32 v107, v212
	v_mov_b32_e32 v109, v213
	v_mov_b32_e32 v111, v214
	v_mov_b32_e32 v146, v215
	v_mov_b32_e32 v150, v216
	v_mov_b32_e32 v154, v217
	v_mov_b32_e32 v158, v218
	v_mov_b32_e32 v162, v219
	v_mov_b32_e32 v166, v220
	v_mov_b32_e32 v170, v221
	v_mov_b32_e32 v174, v222
	v_mov_b32_e32 v178, v223
	v_mov_b32_e32 v182, v224
	v_mov_b32_e32 v186, v225
	v_mov_b32_e32 v190, v226
	v_mov_b32_e32 v194, v227
	v_mov_b32_e32 v110, v242
	v_mov_b32_e32 v108, v243
	v_lshlrev_b32_e32 v120, 16, v86
	v_and_b32_e32 v121, 0xffff0000, v86
	v_lshlrev_b32_e32 v86, 16, v87
	v_and_b32_e32 v87, 0xffff0000, v87
	v_lshlrev_b32_e32 v122, 16, v88
	v_and_b32_e32 v123, 0xffff0000, v88
	v_lshlrev_b32_e32 v88, 16, v89
	v_and_b32_e32 v89, 0xffff0000, v89
	v_lshlrev_b32_e32 v124, 16, v90
	v_and_b32_e32 v125, 0xffff0000, v90
	v_lshlrev_b32_e32 v90, 16, v91
	v_and_b32_e32 v91, 0xffff0000, v91
	v_lshlrev_b32_e32 v126, 16, v92
	v_and_b32_e32 v127, 0xffff0000, v92
	v_lshlrev_b32_e32 v130, 16, v96
	v_and_b32_e32 v131, 0xffff0000, v96
	v_lshlrev_b32_e32 v134, 16, v118
	v_and_b32_e32 v135, 0xffff0000, v118
	v_lshlrev_b32_e32 v128, 16, v94
	v_and_b32_e32 v129, 0xffff0000, v94
	v_lshlrev_b32_e32 v132, 16, v116
	v_and_b32_e32 v133, 0xffff0000, v116
	v_lshlrev_b32_e32 v118, 16, v119
	v_and_b32_e32 v119, 0xffff0000, v119
	v_lshlrev_b32_e32 v92, 16, v93
	v_and_b32_e32 v93, 0xffff0000, v93
	v_lshlrev_b32_e32 v96, 16, v97
	v_and_b32_e32 v97, 0xffff0000, v97
	v_lshlrev_b32_e32 v94, 16, v95
	v_and_b32_e32 v95, 0xffff0000, v95
	v_lshlrev_b32_e32 v116, 16, v117
	v_and_b32_e32 v117, 0xffff0000, v117
	v_cvt_pk_f32_fp8_e32 v[112:113], v107
	v_cvt_pk_f32_fp8_e32 v[136:137], v109
	v_cvt_pk_f32_fp8_sdwa v[138:139], v109 src0_sel:WORD_1
	v_cvt_pk_f32_fp8_e32 v[144:145], v146
	v_cvt_pk_f32_fp8_sdwa v[146:147], v146 src0_sel:WORD_1
	v_cvt_pk_f32_fp8_sdwa v[114:115], v107 src0_sel:WORD_1
	v_cvt_pk_f32_fp8_e32 v[140:141], v111
	v_cvt_pk_f32_fp8_sdwa v[142:143], v111 src0_sel:WORD_1
	v_cvt_pk_f32_fp8_e32 v[152:153], v154
	v_cvt_pk_f32_fp8_sdwa v[154:155], v154 src0_sel:WORD_1
	v_cvt_pk_f32_fp8_e32 v[160:161], v162
	v_cvt_pk_f32_fp8_sdwa v[162:163], v162 src0_sel:WORD_1
	v_cvt_pk_f32_fp8_e32 v[168:169], v170
	v_cvt_pk_f32_fp8_sdwa v[170:171], v170 src0_sel:WORD_1
	v_cvt_pk_f32_fp8_e32 v[176:177], v178
	v_cvt_pk_f32_fp8_sdwa v[178:179], v178 src0_sel:WORD_1
	v_cvt_pk_f32_fp8_e32 v[184:185], v186
	v_cvt_pk_f32_fp8_sdwa v[186:187], v186 src0_sel:WORD_1
	v_cvt_pk_f32_fp8_e32 v[192:193], v194
	v_cvt_pk_f32_fp8_sdwa v[194:195], v194 src0_sel:WORD_1
	v_cvt_pk_f32_fp8_e32 v[148:149], v150
	v_cvt_pk_f32_fp8_sdwa v[150:151], v150 src0_sel:WORD_1
	v_cvt_pk_f32_fp8_e32 v[156:157], v158
	v_cvt_pk_f32_fp8_e32 v[172:173], v174
	v_cvt_pk_f32_fp8_e32 v[188:189], v190
	v_cvt_pk_f32_fp8_sdwa v[158:159], v158 src0_sel:WORD_1
	v_cvt_pk_f32_fp8_e32 v[164:165], v166
	v_cvt_pk_f32_fp8_sdwa v[166:167], v166 src0_sel:WORD_1
	v_cvt_pk_f32_fp8_sdwa v[174:175], v174 src0_sel:WORD_1
	v_cvt_pk_f32_fp8_e32 v[180:181], v182
	v_cvt_pk_f32_fp8_sdwa v[182:183], v182 src0_sel:WORD_1
	v_cvt_pk_f32_fp8_sdwa v[190:191], v190 src0_sel:WORD_1
	v_pk_mul_f32 v[138:139], v[108:109], v[138:139] op_sel_hi:[0,1]
	v_pk_mul_f32 v[136:137], v[108:109], v[136:137] op_sel_hi:[0,1]
	v_pk_mul_f32 v[146:147], v[108:109], v[146:147] op_sel_hi:[0,1]
	v_pk_mul_f32 v[144:145], v[108:109], v[144:145] op_sel_hi:[0,1]
	v_pk_mul_f32 v[152:153], v[108:109], v[152:153] op_sel_hi:[0,1]
	v_pk_mul_f32 v[154:155], v[108:109], v[154:155] op_sel_hi:[0,1]
	v_pk_mul_f32 v[162:163], v[108:109], v[162:163] op_sel_hi:[0,1]
	v_pk_mul_f32 v[160:161], v[108:109], v[160:161] op_sel_hi:[0,1]
	v_pk_mul_f32 v[170:171], v[108:109], v[170:171] op_sel_hi:[0,1]
	v_pk_mul_f32 v[168:169], v[108:109], v[168:169] op_sel_hi:[0,1]
	v_pk_mul_f32 v[176:177], v[108:109], v[176:177] op_sel_hi:[0,1]
	v_pk_mul_f32 v[178:179], v[108:109], v[178:179] op_sel_hi:[0,1]
	v_pk_mul_f32 v[186:187], v[108:109], v[186:187] op_sel_hi:[0,1]
	v_pk_mul_f32 v[184:185], v[108:109], v[184:185] op_sel_hi:[0,1]
	v_pk_mul_f32 v[194:195], v[108:109], v[194:195] op_sel_hi:[0,1]
	v_pk_mul_f32 v[108:109], v[108:109], v[192:193] op_sel_hi:[0,1]
	v_pk_fma_f32 v[112:113], v[110:111], v[112:113], v[136:137] op_sel_hi:[0,1,1]
	v_pk_fma_f32 v[114:115], v[110:111], v[114:115], v[138:139] op_sel_hi:[0,1,1]
	v_pk_fma_f32 v[136:137], v[110:111], v[140:141], v[144:145] op_sel_hi:[0,1,1]
	v_pk_fma_f32 v[138:139], v[110:111], v[142:143], v[146:147] op_sel_hi:[0,1,1]
	v_pk_fma_f32 v[140:141], v[110:111], v[150:151], v[154:155] op_sel_hi:[0,1,1]
	v_pk_fma_f32 v[142:143], v[110:111], v[148:149], v[152:153] op_sel_hi:[0,1,1]
	v_pk_fma_f32 v[144:145], v[110:111], v[156:157], v[160:161] op_sel_hi:[0,1,1]
	v_pk_fma_f32 v[154:155], v[110:111], v[172:173], v[176:177] op_sel_hi:[0,1,1]
	v_pk_fma_f32 v[108:109], v[110:111], v[188:189], v[108:109] op_sel_hi:[0,1,1]
	v_pk_fma_f32 v[86:87], v[10:11], v[114:115], v[86:87]
	v_pk_fma_f32 v[112:113], v[8:9], v[112:113], v[120:121]
	v_pk_fma_f32 v[88:89], v[14:15], v[138:139], v[88:89]
	v_pk_fma_f32 v[114:115], v[12:13], v[136:137], v[122:123]
	v_pk_fma_f32 v[146:147], v[110:111], v[158:159], v[162:163] op_sel_hi:[0,1,1]
	v_pk_fma_f32 v[148:149], v[110:111], v[164:165], v[168:169] op_sel_hi:[0,1,1]
	v_pk_fma_f32 v[150:151], v[110:111], v[166:167], v[170:171] op_sel_hi:[0,1,1]
; __device__ __forceinline__ void phase12(const Args& a, unsigned char* lds_g, int lane, int wave) {
;     ...
;             f32x4 y; y.x = w0 * l0[0] + w1 * l1[0]; y.y = w0 * l0[1] + w1 * l1[1]; y.z = w0 * h0[0] + w1 * h1[0]; y.w = w0 * h0[1] + w1 * h1[1];
;             const unsigned long long xw = xr[64 * j];
;             v[j] = (f32x4){bflo((unsigned)xw), bfhi((unsigned)xw), bflo((unsigned)(xw >> 32)), bfhi((unsigned)(xw >> 32))} + g2 * y;
;             s += (v[j].x * v[j].x + v[j].y * v[j].y) + (v[j].z * v[j].z + v[j].w * v[j].w);
;         }
	v_pk_fma_f32 v[152:153], v[110:111], v[174:175], v[178:179] op_sel_hi:[0,1,1]
	v_pk_fma_f32 v[156:157], v[110:111], v[180:181], v[184:185] op_sel_hi:[0,1,1]
	v_pk_fma_f32 v[158:159], v[110:111], v[182:183], v[186:187] op_sel_hi:[0,1,1]
	v_pk_fma_f32 v[110:111], v[110:111], v[190:191], v[194:195] op_sel_hi:[0,1,1]
	v_pk_fma_f32 v[120:121], v[20:21], v[142:143], v[124:125]
	v_pk_fma_f32 v[90:91], v[22:23], v[140:141], v[90:91]
	v_pk_fma_f32 v[122:123], v[28:29], v[144:145], v[126:127]
	v_pk_fma_f32 v[126:127], v[44:45], v[154:155], v[130:131]
	v_pk_fma_f32 v[108:109], v[60:61], v[108:109], v[134:135]
	v_mov_b32_e32 v130, v113
	v_mov_b32_e32 v131, v115
	v_mov_b32_e32 v134, v87
	v_mov_b32_e32 v135, v89
	v_pk_fma_f32 v[124:125], v[36:37], v[148:149], v[128:129]
	v_pk_fma_f32 v[128:129], v[52:53], v[156:157], v[132:133]
	v_pk_fma_f32 v[110:111], v[62:63], v[110:111], v[118:119]
	v_mov_b32_e32 v118, v112
	v_mov_b32_e32 v119, v114
	v_mov_b32_e32 v132, v86
	v_mov_b32_e32 v133, v88
	v_pk_mul_f32 v[136:137], v[90:91], v[90:91]
	v_pk_mul_f32 v[138:139], v[120:121], v[120:121]
	v_pk_mul_f32 v[130:131], v[130:131], v[130:131]
	v_pk_mul_f32 v[134:135], v[134:135], v[134:135]
	v_pk_fma_f32 v[92:93], v[30:31], v[146:147], v[92:93]
	v_pk_fma_f32 v[96:97], v[46:47], v[152:153], v[96:97]
	v_pk_mov_b32 v[152:153], v[138:139], v[136:137] op_sel:[1,0]
	v_mov_b32_e32 v139, v137
	v_pk_fma_f32 v[118:119], v[118:119], v[118:119], v[130:131]
	v_pk_fma_f32 v[130:131], v[132:133], v[132:133], v[134:135]
	v_pk_fma_f32 v[94:95], v[38:39], v[150:151], v[94:95]
	v_mul_f32_e32 v140, v123, v123
	v_mul_f32_e32 v142, v93, v93
	v_pk_add_f32 v[132:133], v[152:153], v[138:139]
	v_pk_add_f32 v[118:119], v[118:119], v[130:131]
	v_mul_f32_e32 v107, v124, v124
	v_mul_f32_e32 v151, v125, v125
	v_mul_f32_e32 v154, v94, v94
	v_mul_f32_e32 v155, v95, v95
	v_pk_fma_f32 v[136:137], v[122:123], v[122:123], v[140:141] op_sel_hi:[1,1,0]
	v_pk_fma_f32 v[140:141], v[92:93], v[92:93], v[142:143] op_sel_hi:[1,1,0]
	v_pk_add_f32 v[130:131], v[132:133], v[132:133] op_sel:[0,1] op_sel_hi:[1,0]
	v_pk_add_f32 v[118:119], v[118:119], v[118:119] op_sel:[0,1] op_sel_hi:[1,0]
	v_pk_mul_f32 v[144:145], v[96:97], v[96:97]
	v_pk_mul_f32 v[146:147], v[126:127], v[126:127]
	v_mov_b32_e32 v137, v154
	v_mov_b32_e32 v141, v155
	v_mov_b32_e32 v131, v151
	v_mov_b32_e32 v119, v107
	v_pk_fma_f32 v[116:117], v[54:55], v[158:159], v[116:117]
	v_pk_mov_b32 v[142:143], v[146:147], v[144:145] op_sel:[1,0]
	v_mov_b32_e32 v147, v145
	v_pk_add_f32 v[132:133], v[136:137], v[140:141]
	v_pk_add_f32 v[118:119], v[118:119], v[130:131]
	v_mul_f32_e32 v148, v129, v129
	v_mul_f32_e32 v150, v117, v117
	v_pk_add_f32 v[134:135], v[142:143], v[146:147]
	v_pk_add_f32 v[118:119], v[118:119], v[132:133]
	v_mul_f32_e32 v156, v108, v108
	v_mul_f32_e32 v157, v109, v109
	v_mul_f32_e32 v158, v110, v110
	v_mul_f32_e32 v159, v111, v111
	v_pk_fma_f32 v[144:145], v[128:129], v[128:129], v[148:149] op_sel_hi:[1,1,0]
	v_pk_fma_f32 v[148:149], v[116:117], v[116:117], v[150:151] op_sel_hi:[1,1,0]
	v_pk_add_f32 v[134:135], v[134:135], v[134:135] op_sel:[0,1] op_sel_hi:[1,0]
	v_pk_add_f32 v[118:119], v[118:119], v[118:119] op_sel:[0,1] op_sel_hi:[1,0]
	v_mov_b32_e32 v145, v158
	v_mov_b32_e32 v149, v159
	v_mov_b32_e32 v135, v157
	v_mov_b32_e32 v119, v156
	v_pk_add_f32 v[136:137], v[144:145], v[148:149]
	v_pk_add_f32 v[118:119], v[118:119], v[134:135]
	s_nop 0
	v_pk_add_f32 v[118:119], v[118:119], v[136:137]
	s_nop 0
	v_add_f32_e32 v107, v118, v119
	ds_bpermute_b32 v118, v99, v107
	s_waitcnt lgkmcnt(0)
	v_add_f32_e32 v107, v107, v118
	ds_bpermute_b32 v118, v100, v107
	s_waitcnt lgkmcnt(0)
	v_add_f32_e32 v107, v107, v118
	ds_bpermute_b32 v118, v101, v107
	s_waitcnt lgkmcnt(0)
	v_add_f32_e32 v107, v107, v118
	ds_bpermute_b32 v118, v102, v107
	s_waitcnt lgkmcnt(0)
; __device__ __forceinline__ void phase12(const Args& a, unsigned char* lds_g, int lane, int wave) {
;     ...
;     for (int t0 = 4 * gw; t0 < NLAT; t0 += 4 * NGW) {
;     ...
;         }
;         const float rstd = 1.f / sqrtf(wave_sum(s) * (1.f / D) + EPS);
;         f32x4* o = (f32x4*)(a.out + (size_t)t * D) + lane;
; #pragma unroll
;         for (int j = 0; j < 8; ++j) o[64 * j] = v[j] * rstd * fgv[j];
;       }
;     }
	v_add_f32_e32 v107, v107, v118
	ds_bpermute_b32 v118, v103, v107
	s_waitcnt lgkmcnt(0)
	v_add_f32_e32 v107, v107, v118
	ds_bpermute_b32 v118, v104, v107
	s_waitcnt lgkmcnt(0)
	v_add_f32_e32 v107, v107, v118
	v_fmamk_f32 v107, v107, 0x3a000000, v105
	v_mul_f32_e32 v118, 0x4f800000, v107
	v_cmp_gt_f32_e32 vcc, s11, v107
	s_nop 1
	v_cndmask_b32_e32 v107, v107, v118, vcc
	v_sqrt_f32_e32 v118, v107
	s_nop 0
	v_add_u32_e32 v119, -1, v118
	v_add_u32_e32 v130, 1, v118
	v_fma_f32 v131, -v119, v118, v107
	v_fma_f32 v132, -v130, v118, v107
	v_cmp_ge_f32_e64 s[0:1], 0, v131
	s_nop 1
	v_cndmask_b32_e64 v118, v118, v119, s[0:1]
	v_cmp_lt_f32_e64 s[0:1], 0, v132
	s_nop 1
	v_cndmask_b32_e64 v118, v118, v130, s[0:1]
	v_mul_f32_e32 v119, 0x37800000, v118
	v_cndmask_b32_e32 v118, v118, v119, vcc
	v_cmp_class_f32_e32 vcc, v107, v106
	s_nop 1
	v_cndmask_b32_e32 v107, v118, v107, vcc
	v_div_scale_f32 v118, s[0:1], v107, v107, 1.0
	v_rcp_f32_e32 v130, v118
	v_div_scale_f32 v119, vcc, 1.0, v107, 1.0
	v_fma_f32 v131, -v118, v130, 1.0
	v_fmac_f32_e32 v130, v131, v130
	v_mul_f32_e32 v131, v119, v130
	v_fma_f32 v132, -v118, v131, v119
	v_fmac_f32_e32 v131, v132, v130
	v_fma_f32 v118, -v118, v131, v119
	v_div_fmas_f32 v118, v118, v130, v131
	v_div_fixup_f32 v118, v118, v107, 1.0
	v_pk_mul_f32 v[112:113], v[112:113], v[118:119] op_sel_hi:[1,0]
	v_pk_mul_f32 v[86:87], v[86:87], v[118:119] op_sel_hi:[1,0]
	v_pk_mul_f32 v[114:115], v[114:115], v[118:119] op_sel_hi:[1,0]
	v_pk_mul_f32 v[130:131], v[88:89], v[118:119] op_sel_hi:[1,0]
	v_pk_mul_f32 v[120:121], v[120:121], v[118:119] op_sel_hi:[1,0]
	v_pk_mul_f32 v[132:133], v[90:91], v[118:119] op_sel_hi:[1,0]
	v_pk_mul_f32 v[122:123], v[122:123], v[118:119] op_sel_hi:[1,0]
	v_pk_mul_f32 v[134:135], v[92:93], v[118:119] op_sel_hi:[1,0]
	v_pk_mul_f32 v[124:125], v[124:125], v[118:119] op_sel_hi:[1,0]
	v_pk_mul_f32 v[136:137], v[94:95], v[118:119] op_sel_hi:[1,0]
	v_pk_mul_f32 v[126:127], v[126:127], v[118:119] op_sel_hi:[1,0]
	v_pk_mul_f32 v[138:139], v[96:97], v[118:119] op_sel_hi:[1,0]
	v_pk_mul_f32 v[128:129], v[128:129], v[118:119] op_sel_hi:[1,0]
	v_pk_mul_f32 v[140:141], v[116:117], v[118:119] op_sel_hi:[1,0]
	v_pk_mul_f32 v[142:143], v[108:109], v[118:119] op_sel_hi:[1,0]
	v_pk_mul_f32 v[144:145], v[110:111], v[118:119] op_sel_hi:[1,0]
	v_pk_mul_f32 v[88:89], v[2:3], v[86:87]
	v_pk_mul_f32 v[86:87], v[0:1], v[112:113]
	v_pk_mul_f32 v[92:93], v[6:7], v[130:131]
	v_pk_mul_f32 v[90:91], v[4:5], v[114:115]
	v_pk_mul_f32 v[96:97], v[18:19], v[132:133]
	v_pk_mul_f32 v[94:95], v[16:17], v[120:121]
	v_pk_mul_f32 v[110:111], v[26:27], v[134:135]
	v_pk_mul_f32 v[108:109], v[24:25], v[122:123]
	v_pk_mul_f32 v[114:115], v[34:35], v[136:137]
	v_pk_mul_f32 v[112:113], v[32:33], v[124:125]
	v_pk_mul_f32 v[118:119], v[42:43], v[138:139]
	v_pk_mul_f32 v[116:117], v[40:41], v[126:127]
	v_pk_mul_f32 v[122:123], v[50:51], v[140:141]
	v_pk_mul_f32 v[120:121], v[48:49], v[128:129]
	v_pk_mul_f32 v[126:127], v[58:59], v[144:145]
	v_pk_mul_f32 v[124:125], v[56:57], v[142:143]
	global_store_dwordx4 v[84:85], v[86:89], off offset:-4096 sc0 sc1
	global_store_dwordx4 v[84:85], v[90:93], off offset:-3072 sc0 sc1
	global_store_dwordx4 v[84:85], v[94:97], off offset:-2048 sc0 sc1
	global_store_dwordx4 v[84:85], v[108:111], off offset:-1024 sc0 sc1
	global_store_dwordx4 v[84:85], v[112:115], off sc0 sc1
	global_store_dwordx4 v[84:85], v[116:119], off offset:1024 sc0 sc1
	global_store_dwordx4 v[84:85], v[120:123], off offset:2048 sc0 sc1
	global_store_dwordx4 v[84:85], v[124:127], off offset:3072 sc0 sc1
	v_lshl_add_u64 v[84:85], v[84:85], 0, s[18:19]
	s_add_i32 s8, s8, s10
	s_add_i32 s26, s26, s10
	s_add_i32 s27, s27, s28
	v_lshl_add_u64 v[78:79], v[78:79], 0, s[2:3]
	s_cmpk_gt_i32 s8, 0x1fff
	v_lshl_add_u64 v[80:81], v[80:81], 0, s[14:15]
	s_cbranch_scc0 .LBB0_1274
